# GEMM loops: priority inverted - load segments (ds_read + LDS-DMA issue) run at s_setprio 1, MFMA blocks at 0
# baseline (speedup 1.0000x reference)
.LBB0_261:
	ds_read_b128 v[144:147], v170
	ds_read_b128 v[148:151], v170 offset:1024
	ds_read_b128 v[174:177], v170 offset:2048
	ds_read_b128 v[178:181], v170 offset:3072
	ds_read_b128 v[182:185], v171
	ds_read_b128 v[186:189], v171 offset:1024
	ds_read_b128 v[190:193], v171 offset:2048
	ds_read_b128 v[194:197], v171 offset:3072
	s_add_u32 s26, s80, 0xfff80080
	s_addc_u32 s27, s81, -1
	s_cmp_eq_u32 vcc_hi, 28
	s_cselect_b32 s83, s69, s27
	s_cselect_b32 s82, s75, s26
	s_cselect_b32 s27, s57, vcc_lo
	s_cselect_b32 s26, s96, s97
	v_lshl_add_u64 v[152:153], s[80:81], 0, v[134:135]
	s_add_i32 m0, s87, 0xc000
	ds_read_b128 v[198:201], v172
	ds_read_b128 v[202:205], v172 offset:1024
	ds_read_b128 v[206:209], v172 offset:2048
	ds_read_b128 v[210:213], v172 offset:3072
	ds_read_b128 v[214:217], v172 offset:4096
	ds_read_b128 v[220:223], v172 offset:5120
	ds_read_b128 v[224:227], v172 offset:6144
	ds_read_b128 v[228:231], v172 offset:7168
	global_load_lds_dwordx4 v[152:153], off
	v_lshl_add_u64 v[152:153], s[80:81], 0, v[138:139]
	s_add_i32 m0, s87, 0xe000
	s_nop 0
	global_load_lds_dwordx4 v[152:153], off
	s_waitcnt vmcnt(8)
	s_waitcnt lgkmcnt(0)
	s_barrier
	s_setprio 0
	s_waitcnt lgkmcnt(0)
	v_mfma_f32_16x16x32_bf16 v[122:125], v[144:147], v[198:201], v[122:125]
	v_mfma_f32_16x16x32_bf16 v[118:121], v[174:177], v[198:201], v[118:121]
	v_mfma_f32_16x16x32_bf16 v[106:109], v[144:147], v[206:209], v[106:109]
	v_mfma_f32_16x16x32_bf16 v[102:105], v[174:177], v[206:209], v[102:105]
	v_mfma_f32_16x16x32_bf16 v[90:93], v[144:147], v[214:217], v[90:93]
	v_mfma_f32_16x16x32_bf16 v[86:89], v[174:177], v[214:217], v[86:89]
	v_mfma_f32_16x16x32_bf16 v[74:77], v[144:147], v[224:227], v[74:77]
	v_mfma_f32_16x16x32_bf16 v[70:73], v[174:177], v[224:227], v[70:73]
	v_mfma_f32_16x16x32_bf16 v[122:125], v[148:151], v[202:205], v[122:125]
	v_mfma_f32_16x16x32_bf16 v[118:121], v[178:181], v[202:205], v[118:121]
	v_mfma_f32_16x16x32_bf16 v[106:109], v[148:151], v[210:213], v[106:109]
	v_mfma_f32_16x16x32_bf16 v[102:105], v[178:181], v[210:213], v[102:105]
	v_mfma_f32_16x16x32_bf16 v[90:93], v[148:151], v[220:223], v[90:93]
	v_mfma_f32_16x16x32_bf16 v[86:89], v[178:181], v[220:223], v[86:89]
	v_mfma_f32_16x16x32_bf16 v[74:77], v[148:151], v[228:231], v[74:77]
	v_mfma_f32_16x16x32_bf16 v[70:73], v[178:181], v[228:231], v[70:73]
	v_mfma_f32_16x16x32_bf16 v[126:129], v[182:185], v[198:201], v[126:129]
	v_mfma_f32_16x16x32_bf16 v[114:117], v[190:193], v[198:201], v[114:117]
	v_mfma_f32_16x16x32_bf16 v[110:113], v[182:185], v[206:209], v[110:113]
	v_mfma_f32_16x16x32_bf16 v[98:101], v[190:193], v[206:209], v[98:101]
	v_mfma_f32_16x16x32_bf16 v[94:97], v[182:185], v[214:217], v[94:97]
	v_mfma_f32_16x16x32_bf16 v[82:85], v[190:193], v[214:217], v[82:85]
	v_mfma_f32_16x16x32_bf16 v[78:81], v[182:185], v[224:227], v[78:81]
	v_mfma_f32_16x16x32_bf16 v[66:69], v[190:193], v[224:227], v[66:69]
	v_mfma_f32_16x16x32_bf16 v[126:129], v[186:189], v[202:205], v[126:129]
	v_mfma_f32_16x16x32_bf16 v[114:117], v[194:197], v[202:205], v[114:117]
	v_mfma_f32_16x16x32_bf16 v[110:113], v[186:189], v[210:213], v[110:113]
	v_mfma_f32_16x16x32_bf16 v[98:101], v[194:197], v[210:213], v[98:101]
	v_mfma_f32_16x16x32_bf16 v[94:97], v[186:189], v[220:223], v[94:97]
	v_mfma_f32_16x16x32_bf16 v[82:85], v[194:197], v[220:223], v[82:85]
	v_mfma_f32_16x16x32_bf16 v[78:81], v[186:189], v[228:231], v[78:81]
	v_mfma_f32_16x16x32_bf16 v[66:69], v[194:197], v[228:231], v[66:69]
	s_setprio 1
	s_barrier
	v_lshl_add_u64 v[152:153], s[26:27], 0, v[162:163]
	s_add_i32 s26, s94, s86
	s_mov_b32 m0, s26
	ds_read_b128 v[198:201], v172 offset:16384
	ds_read_b128 v[202:205], v172 offset:17408
	ds_read_b128 v[206:209], v172 offset:18432
	ds_read_b128 v[210:213], v172 offset:19456
	ds_read_b128 v[214:217], v172 offset:20480
	ds_read_b128 v[220:223], v172 offset:21504
	ds_read_b128 v[224:227], v172 offset:22528
	ds_read_b128 v[228:231], v172 offset:23552
	global_load_lds_dwordx4 v[152:153], off
	v_lshl_add_u64 v[232:233], v[152:153], 0, s[10:11]
	s_add_i32 m0, s26, 0x2000
	s_add_i32 s26, s95, s86
	global_load_lds_dwordx4 v[232:233], off
	v_lshl_add_u64 v[232:233], v[152:153], 0, s[12:13]
	s_mov_b32 m0, s26
	v_lshl_add_u64 v[234:235], s[82:83], 0, v[132:133]
	global_load_lds_dwordx4 v[232:233], off
	v_lshl_add_u64 v[232:233], v[152:153], 0, s[14:15]
	s_add_i32 m0, s26, 0x2000
	s_nop 0
	global_load_lds_dwordx4 v[232:233], off
	v_lshl_add_u64 v[232:233], s[82:83], 0, v[130:131]
	s_mov_b32 m0, s87
	s_nop 0
	global_load_lds_dwordx4 v[232:233], off
	s_mov_b32 m0, s88
	s_nop 0
	global_load_lds_dwordx4 v[234:235], off
	s_waitcnt vmcnt(8)
	s_waitcnt lgkmcnt(0)
	s_barrier
	s_setprio 0
	s_waitcnt lgkmcnt(0)
	v_mfma_f32_16x16x32_bf16 v[58:61], v[144:147], v[198:201], v[58:61]
	v_mfma_f32_16x16x32_bf16 v[54:57], v[174:177], v[198:201], v[54:57]
	v_mfma_f32_16x16x32_bf16 v[42:45], v[144:147], v[206:209], v[42:45]
	v_mfma_f32_16x16x32_bf16 v[38:41], v[174:177], v[206:209], v[38:41]
	v_mfma_f32_16x16x32_bf16 v[26:29], v[144:147], v[214:217], v[26:29]
	v_mfma_f32_16x16x32_bf16 v[22:25], v[174:177], v[214:217], v[22:25]
	v_mfma_f32_16x16x32_bf16 v[10:13], v[144:147], v[224:227], v[10:13]
	v_mfma_f32_16x16x32_bf16 v[6:9], v[174:177], v[224:227], v[6:9]
	v_mfma_f32_16x16x32_bf16 v[58:61], v[148:151], v[202:205], v[58:61]
	v_mfma_f32_16x16x32_bf16 v[54:57], v[178:181], v[202:205], v[54:57]
	v_mfma_f32_16x16x32_bf16 v[42:45], v[148:151], v[210:213], v[42:45]
	v_mfma_f32_16x16x32_bf16 v[38:41], v[178:181], v[210:213], v[38:41]
	v_mfma_f32_16x16x32_bf16 v[26:29], v[148:151], v[220:223], v[26:29]
	v_mfma_f32_16x16x32_bf16 v[22:25], v[178:181], v[220:223], v[22:25]
	v_mfma_f32_16x16x32_bf16 v[10:13], v[148:151], v[228:231], v[10:13]
	v_mfma_f32_16x16x32_bf16 v[6:9], v[178:181], v[228:231], v[6:9]
	v_mfma_f32_16x16x32_bf16 v[62:65], v[182:185], v[198:201], v[62:65]
	v_mfma_f32_16x16x32_bf16 v[50:53], v[190:193], v[198:201], v[50:53]
	v_mfma_f32_16x16x32_bf16 v[46:49], v[182:185], v[206:209], v[46:49]
	v_mfma_f32_16x16x32_bf16 v[34:37], v[190:193], v[206:209], v[34:37]
	v_mfma_f32_16x16x32_bf16 v[30:33], v[182:185], v[214:217], v[30:33]
	v_mfma_f32_16x16x32_bf16 v[18:21], v[190:193], v[214:217], v[18:21]
	v_mfma_f32_16x16x32_bf16 v[14:17], v[182:185], v[224:227], v[14:17]
	v_mfma_f32_16x16x32_bf16 v[2:5], v[190:193], v[224:227], v[2:5]
	v_mfma_f32_16x16x32_bf16 v[62:65], v[186:189], v[202:205], v[62:65]
	v_mfma_f32_16x16x32_bf16 v[50:53], v[194:197], v[202:205], v[50:53]
	v_mfma_f32_16x16x32_bf16 v[46:49], v[186:189], v[210:213], v[46:49]
	v_mfma_f32_16x16x32_bf16 v[34:37], v[194:197], v[210:213], v[34:37]
	v_mfma_f32_16x16x32_bf16 v[30:33], v[186:189], v[220:223], v[30:33]
	v_mfma_f32_16x16x32_bf16 v[18:21], v[194:197], v[220:223], v[18:21]
	v_mfma_f32_16x16x32_bf16 v[14:17], v[186:189], v[228:231], v[14:17]
	v_mfma_f32_16x16x32_bf16 v[2:5], v[194:197], v[228:231], v[2:5]
	s_setprio 1
	s_barrier
	s_add_i32 s33, 0, 0x18000
	v_add_u32_e32 v136, s33, v167
	s_add_i32 s8, 0, 0x1c000
	ds_read_b128 v[144:147], v136
	ds_read_b128 v[148:151], v136 offset:1024
	ds_read_b128 v[174:177], v136 offset:2048
	ds_read_b128 v[178:181], v136 offset:3072
	v_add_u32_e32 v136, s8, v167
	ds_read_b128 v[182:185], v136
	ds_read_b128 v[186:189], v136 offset:1024
	ds_read_b128 v[190:193], v136 offset:2048
	ds_read_b128 v[194:197], v136 offset:3072
	s_add_u32 s26, s82, 0x80000
	s_addc_u32 s27, s83, 0
	s_mov_b32 m0, s89
	v_lshl_add_u64 v[236:237], s[26:27], 0, v[130:131]
	ds_read_b128 v[198:201], v172 offset:32768
	ds_read_b128 v[202:205], v172 offset:33792
	ds_read_b128 v[206:209], v172 offset:34816
	ds_read_b128 v[210:213], v172 offset:35840
	ds_read_b128 v[214:217], v172 offset:36864
	ds_read_b128 v[220:223], v172 offset:37888
	ds_read_b128 v[224:227], v172 offset:38912
	ds_read_b128 v[228:231], v172 offset:39936
	global_load_lds_dwordx4 v[236:237], off
	v_lshl_add_u64 v[236:237], s[26:27], 0, v[132:133]
	s_mov_b32 m0, s90
	s_nop 0
	global_load_lds_dwordx4 v[236:237], off
	s_waitcnt vmcnt(8)
	s_waitcnt lgkmcnt(0)
	s_barrier
	s_setprio 0
	s_waitcnt lgkmcnt(0)
	v_mfma_f32_16x16x32_bf16 v[122:125], v[144:147], v[198:201], v[122:125]
	v_mfma_f32_16x16x32_bf16 v[118:121], v[174:177], v[198:201], v[118:121]
	v_mfma_f32_16x16x32_bf16 v[106:109], v[144:147], v[206:209], v[106:109]
	v_mfma_f32_16x16x32_bf16 v[102:105], v[174:177], v[206:209], v[102:105]
	v_mfma_f32_16x16x32_bf16 v[90:93], v[144:147], v[214:217], v[90:93]
	v_mfma_f32_16x16x32_bf16 v[86:89], v[174:177], v[214:217], v[86:89]
	v_mfma_f32_16x16x32_bf16 v[74:77], v[144:147], v[224:227], v[74:77]
	v_mfma_f32_16x16x32_bf16 v[70:73], v[174:177], v[224:227], v[70:73]
	v_mfma_f32_16x16x32_bf16 v[122:125], v[148:151], v[202:205], v[122:125]
	v_mfma_f32_16x16x32_bf16 v[118:121], v[178:181], v[202:205], v[118:121]
	v_mfma_f32_16x16x32_bf16 v[106:109], v[148:151], v[210:213], v[106:109]
	v_mfma_f32_16x16x32_bf16 v[102:105], v[178:181], v[210:213], v[102:105]
	v_mfma_f32_16x16x32_bf16 v[90:93], v[148:151], v[220:223], v[90:93]
	v_mfma_f32_16x16x32_bf16 v[86:89], v[178:181], v[220:223], v[86:89]
	v_mfma_f32_16x16x32_bf16 v[74:77], v[148:151], v[228:231], v[74:77]
	v_mfma_f32_16x16x32_bf16 v[70:73], v[178:181], v[228:231], v[70:73]
	v_mfma_f32_16x16x32_bf16 v[126:129], v[182:185], v[198:201], v[126:129]
	v_mfma_f32_16x16x32_bf16 v[114:117], v[190:193], v[198:201], v[114:117]
	v_mfma_f32_16x16x32_bf16 v[110:113], v[182:185], v[206:209], v[110:113]
	v_mfma_f32_16x16x32_bf16 v[98:101], v[190:193], v[206:209], v[98:101]
	v_mfma_f32_16x16x32_bf16 v[94:97], v[182:185], v[214:217], v[94:97]
	v_mfma_f32_16x16x32_bf16 v[82:85], v[190:193], v[214:217], v[82:85]
	v_mfma_f32_16x16x32_bf16 v[78:81], v[182:185], v[224:227], v[78:81]
	v_mfma_f32_16x16x32_bf16 v[66:69], v[190:193], v[224:227], v[66:69]
	v_mfma_f32_16x16x32_bf16 v[126:129], v[186:189], v[202:205], v[126:129]
	v_mfma_f32_16x16x32_bf16 v[114:117], v[194:197], v[202:205], v[114:117]
	v_mfma_f32_16x16x32_bf16 v[110:113], v[186:189], v[210:213], v[110:113]
	v_mfma_f32_16x16x32_bf16 v[98:101], v[194:197], v[210:213], v[98:101]
	v_mfma_f32_16x16x32_bf16 v[94:97], v[186:189], v[220:223], v[94:97]
	v_mfma_f32_16x16x32_bf16 v[82:85], v[194:197], v[220:223], v[82:85]
	v_mfma_f32_16x16x32_bf16 v[78:81], v[186:189], v[228:231], v[78:81]
	v_mfma_f32_16x16x32_bf16 v[66:69], v[194:197], v[228:231], v[66:69]
	s_setprio 1
	s_barrier
	s_add_i32 s9, s33, s86
	v_lshl_add_u64 v[236:237], v[152:153], 0, s[20:21]
	s_mov_b32 m0, s9
	ds_read_b128 v[198:201], v172 offset:49152
	ds_read_b128 v[202:205], v172 offset:50176
	ds_read_b128 v[206:209], v172 offset:51200
	ds_read_b128 v[210:213], v172 offset:52224
	ds_read_b128 v[214:217], v172 offset:53248
	ds_read_b128 v[220:223], v172 offset:54272
	ds_read_b128 v[224:227], v172 offset:55296
	ds_read_b128 v[228:231], v172 offset:56320
	global_load_lds_dwordx4 v[236:237], off
	v_lshl_add_u64 v[236:237], v[152:153], 0, s[22:23]
	s_add_i32 m0, s9, 0x2000
	s_add_i32 s8, s8, s86
	global_load_lds_dwordx4 v[236:237], off
	v_lshl_add_u64 v[236:237], v[152:153], 0, s[40:41]
	s_mov_b32 m0, s8
	v_lshl_add_u64 v[152:153], v[152:153], 0, s[44:45]
	global_load_lds_dwordx4 v[236:237], off
	s_add_i32 m0, s8, 0x2000
	s_nop 0
	global_load_lds_dwordx4 v[152:153], off
	v_lshl_add_u64 v[152:153], v[232:233], 0, s[24:25]
	s_mov_b32 m0, s91
	s_nop 0
	global_load_lds_dwordx4 v[152:153], off
	v_lshl_add_u64 v[152:153], v[234:235], 0, s[24:25]
	s_mov_b32 m0, s92
	s_nop 0
	global_load_lds_dwordx4 v[152:153], off
	s_waitcnt vmcnt(8)
	s_waitcnt lgkmcnt(0)
	s_barrier
	s_setprio 0
	s_waitcnt lgkmcnt(0)
	v_mfma_f32_16x16x32_bf16 v[58:61], v[144:147], v[198:201], v[58:61]
	v_mfma_f32_16x16x32_bf16 v[54:57], v[174:177], v[198:201], v[54:57]
	v_mfma_f32_16x16x32_bf16 v[42:45], v[144:147], v[206:209], v[42:45]
	v_mfma_f32_16x16x32_bf16 v[38:41], v[174:177], v[206:209], v[38:41]
	v_mfma_f32_16x16x32_bf16 v[26:29], v[144:147], v[214:217], v[26:29]
	v_mfma_f32_16x16x32_bf16 v[22:25], v[174:177], v[214:217], v[22:25]
	v_mfma_f32_16x16x32_bf16 v[10:13], v[144:147], v[224:227], v[10:13]
	v_mfma_f32_16x16x32_bf16 v[6:9], v[174:177], v[224:227], v[6:9]
	v_mfma_f32_16x16x32_bf16 v[58:61], v[148:151], v[202:205], v[58:61]
	v_mfma_f32_16x16x32_bf16 v[54:57], v[178:181], v[202:205], v[54:57]
	v_mfma_f32_16x16x32_bf16 v[42:45], v[148:151], v[210:213], v[42:45]
	v_mfma_f32_16x16x32_bf16 v[38:41], v[178:181], v[210:213], v[38:41]
	v_mfma_f32_16x16x32_bf16 v[26:29], v[148:151], v[220:223], v[26:29]
	v_mfma_f32_16x16x32_bf16 v[22:25], v[178:181], v[220:223], v[22:25]
	v_mfma_f32_16x16x32_bf16 v[10:13], v[148:151], v[228:231], v[10:13]
	v_mfma_f32_16x16x32_bf16 v[6:9], v[178:181], v[228:231], v[6:9]
	v_mfma_f32_16x16x32_bf16 v[62:65], v[182:185], v[198:201], v[62:65]
	v_mfma_f32_16x16x32_bf16 v[50:53], v[190:193], v[198:201], v[50:53]
	v_mfma_f32_16x16x32_bf16 v[46:49], v[182:185], v[206:209], v[46:49]
	v_mfma_f32_16x16x32_bf16 v[34:37], v[190:193], v[206:209], v[34:37]
	v_mfma_f32_16x16x32_bf16 v[30:33], v[182:185], v[214:217], v[30:33]
	v_mfma_f32_16x16x32_bf16 v[18:21], v[190:193], v[214:217], v[18:21]
	v_mfma_f32_16x16x32_bf16 v[14:17], v[182:185], v[224:227], v[14:17]
	v_mfma_f32_16x16x32_bf16 v[2:5], v[190:193], v[224:227], v[2:5]
	v_mfma_f32_16x16x32_bf16 v[62:65], v[186:189], v[202:205], v[62:65]
	v_mfma_f32_16x16x32_bf16 v[50:53], v[194:197], v[202:205], v[50:53]
	v_mfma_f32_16x16x32_bf16 v[46:49], v[186:189], v[210:213], v[46:49]
	v_mfma_f32_16x16x32_bf16 v[34:37], v[194:197], v[210:213], v[34:37]
	v_mfma_f32_16x16x32_bf16 v[30:33], v[186:189], v[220:223], v[30:33]
	v_mfma_f32_16x16x32_bf16 v[18:21], v[194:197], v[220:223], v[18:21]
	v_mfma_f32_16x16x32_bf16 v[14:17], v[186:189], v[228:231], v[14:17]
	v_mfma_f32_16x16x32_bf16 v[2:5], v[194:197], v[228:231], v[2:5]
	s_setprio 1
	s_barrier
	s_add_i32 vcc_hi, vcc_hi, 2
	s_add_u32 s97, s97, 0x10000
	s_addc_u32 vcc_lo, vcc_lo, 0
	s_add_u32 s80, s80, 0x100
	s_addc_u32 s81, s81, 0
	s_cmp_gt_u32 vcc_hi, 29
	s_cbranch_scc0 .LBB0_261
	s_and_b64 vcc, exec, s[50:51]
	s_cbranch_vccz .LBB0_264
	s_barrier

.LBB0_285:
	ds_read_b128 v[26:29], v1
	ds_read_b128 v[30:33], v1 offset:1024
	ds_read_b128 v[18:21], v1 offset:2048
	ds_read_b128 v[22:25], v1 offset:3072
	ds_read_b128 v[10:13], v185
	ds_read_b128 v[14:17], v185 offset:1024
	ds_read_b128 v[2:5], v185 offset:2048
	ds_read_b128 v[6:9], v185 offset:3072
	s_add_u32 s26, s70, 0xfffc0080
	s_addc_u32 s27, s71, -1
	s_cmp_eq_u32 s94, 12
	s_cselect_b32 s73, s51, s27
	s_cselect_b32 s72, s90, s26
	s_cselect_b32 s75, s45, s93
	s_cselect_b32 s74, s91, s92
	v_lshl_add_u64 v[176:177], s[70:71], 0, v[168:169]
	s_add_i32 m0, s33, 0xc000
	ds_read_b128 v[190:193], v186
	ds_read_b128 v[194:197], v186 offset:1024
	ds_read_b128 v[198:201], v186 offset:2048
	ds_read_b128 v[202:205], v186 offset:3072
	ds_read_b128 v[206:209], v186 offset:4096
	ds_read_b128 v[210:213], v186 offset:5120
	ds_read_b128 v[220:223], v186 offset:6144
	ds_read_b128 v[224:227], v186 offset:7168
	global_load_lds_dwordx4 v[176:177], off
	v_lshl_add_u64 v[176:177], s[70:71], 0, v[170:171]
	s_add_i32 m0, s33, 0xe000
	s_nop 0
	global_load_lds_dwordx4 v[176:177], off
	s_waitcnt vmcnt(8)
	s_waitcnt lgkmcnt(0)
	s_barrier
	s_setprio 0
	s_waitcnt lgkmcnt(0)
	v_mfma_scale_f32_16x16x128_f8f6f4 v[158:161], v[26:33], v[190:197], v[158:161], v187, v188 op_sel_hi:[0,0,0]
	v_mfma_scale_f32_16x16x128_f8f6f4 v[154:157], v[18:25], v[190:197], v[154:157], v187, v188 op_sel_hi:[0,0,0]
	v_mfma_scale_f32_16x16x128_f8f6f4 v[150:153], v[26:33], v[198:205], v[150:153], v187, v188 op_sel_hi:[0,0,0]
	v_mfma_scale_f32_16x16x128_f8f6f4 v[142:145], v[18:25], v[198:205], v[142:145], v187, v188 op_sel_hi:[0,0,0]
	v_mfma_scale_f32_16x16x128_f8f6f4 v[134:137], v[26:33], v[206:213], v[134:137], v187, v188 op_sel_hi:[0,0,0]
	v_mfma_scale_f32_16x16x128_f8f6f4 v[126:129], v[18:25], v[206:213], v[126:129], v187, v188 op_sel_hi:[0,0,0]
	v_mfma_scale_f32_16x16x128_f8f6f4 v[118:121], v[26:33], v[220:227], v[118:121], v187, v188 op_sel_hi:[0,0,0]
	v_mfma_scale_f32_16x16x128_f8f6f4 v[110:113], v[18:25], v[220:227], v[110:113], v187, v188 op_sel_hi:[0,0,0]
	v_mfma_scale_f32_16x16x128_f8f6f4 v[146:149], v[10:17], v[190:197], v[146:149], v187, v188 op_sel_hi:[0,0,0]
	v_mfma_scale_f32_16x16x128_f8f6f4 v[138:141], v[2:9], v[190:197], v[138:141], v187, v188 op_sel_hi:[0,0,0]
	v_mfma_scale_f32_16x16x128_f8f6f4 v[130:133], v[10:17], v[198:205], v[130:133], v187, v188 op_sel_hi:[0,0,0]
	v_mfma_scale_f32_16x16x128_f8f6f4 v[122:125], v[2:9], v[198:205], v[122:125], v187, v188 op_sel_hi:[0,0,0]
	v_mfma_scale_f32_16x16x128_f8f6f4 v[114:117], v[10:17], v[206:213], v[114:117], v187, v188 op_sel_hi:[0,0,0]
	v_mfma_scale_f32_16x16x128_f8f6f4 v[106:109], v[2:9], v[206:213], v[106:109], v187, v188 op_sel_hi:[0,0,0]
	v_mfma_scale_f32_16x16x128_f8f6f4 v[102:105], v[10:17], v[220:227], v[102:105], v187, v188 op_sel_hi:[0,0,0]
	v_mfma_scale_f32_16x16x128_f8f6f4 v[98:101], v[2:9], v[220:227], v[98:101], v187, v188 op_sel_hi:[0,0,0]
	s_setprio 1
	s_barrier
	s_add_i32 s26, s88, s80
	v_lshl_add_u64 v[176:177], s[74:75], 0, v[162:163]
	s_mov_b32 m0, s26
	ds_read_b128 v[190:193], v186 offset:16384
	ds_read_b128 v[194:197], v186 offset:17408
	ds_read_b128 v[198:201], v186 offset:18432
	ds_read_b128 v[202:205], v186 offset:19456
	ds_read_b128 v[206:209], v186 offset:20480
	ds_read_b128 v[210:213], v186 offset:21504
	ds_read_b128 v[220:223], v186 offset:22528
	ds_read_b128 v[224:227], v186 offset:23552
	global_load_lds_dwordx4 v[176:177], off
	v_lshl_add_u64 v[178:179], v[176:177], 0, s[8:9]
	s_add_i32 m0, s26, 0x2000
	s_add_i32 s26, s89, s80
	global_load_lds_dwordx4 v[178:179], off
	v_lshl_add_u64 v[178:179], v[176:177], 0, s[10:11]
	s_mov_b32 m0, s26
	v_lshl_add_u64 v[180:181], s[72:73], 0, v[166:167]
	global_load_lds_dwordx4 v[178:179], off
	v_lshl_add_u64 v[178:179], v[176:177], 0, s[12:13]
	s_add_i32 m0, s26, 0x2000
	s_nop 0
	global_load_lds_dwordx4 v[178:179], off
	v_lshl_add_u64 v[178:179], s[72:73], 0, v[164:165]
	s_mov_b32 m0, s33
	s_nop 0
	global_load_lds_dwordx4 v[178:179], off
	s_mov_b32 m0, s69
	s_nop 0
	global_load_lds_dwordx4 v[180:181], off
	s_waitcnt vmcnt(8)
	s_waitcnt lgkmcnt(0)
	s_barrier
	s_setprio 0
	s_waitcnt lgkmcnt(0)
	v_mfma_scale_f32_16x16x128_f8f6f4 v[94:97], v[26:33], v[190:197], v[94:97], v187, v188 op_sel_hi:[0,0,0]
	v_mfma_scale_f32_16x16x128_f8f6f4 v[90:93], v[18:25], v[190:197], v[90:93], v187, v188 op_sel_hi:[0,0,0]
	v_mfma_scale_f32_16x16x128_f8f6f4 v[86:89], v[26:33], v[198:205], v[86:89], v187, v188 op_sel_hi:[0,0,0]
	v_mfma_scale_f32_16x16x128_f8f6f4 v[78:81], v[18:25], v[198:205], v[78:81], v187, v188 op_sel_hi:[0,0,0]
	v_mfma_scale_f32_16x16x128_f8f6f4 v[70:73], v[26:33], v[206:213], v[70:73], v187, v188 op_sel_hi:[0,0,0]
	v_mfma_scale_f32_16x16x128_f8f6f4 v[62:65], v[18:25], v[206:213], v[62:65], v187, v188 op_sel_hi:[0,0,0]
	v_mfma_scale_f32_16x16x128_f8f6f4 v[54:57], v[26:33], v[220:227], v[54:57], v187, v188 op_sel_hi:[0,0,0]
	v_mfma_scale_f32_16x16x128_f8f6f4 v[46:49], v[18:25], v[220:227], v[46:49], v187, v188 op_sel_hi:[0,0,0]
	v_mfma_scale_f32_16x16x128_f8f6f4 v[82:85], v[10:17], v[190:197], v[82:85], v187, v188 op_sel_hi:[0,0,0]
	v_mfma_scale_f32_16x16x128_f8f6f4 v[74:77], v[2:9], v[190:197], v[74:77], v187, v188 op_sel_hi:[0,0,0]
	v_mfma_scale_f32_16x16x128_f8f6f4 v[66:69], v[10:17], v[198:205], v[66:69], v187, v188 op_sel_hi:[0,0,0]
	v_mfma_scale_f32_16x16x128_f8f6f4 v[58:61], v[2:9], v[198:205], v[58:61], v187, v188 op_sel_hi:[0,0,0]
	v_mfma_scale_f32_16x16x128_f8f6f4 v[50:53], v[10:17], v[206:213], v[50:53], v187, v188 op_sel_hi:[0,0,0]
	v_mfma_scale_f32_16x16x128_f8f6f4 v[42:45], v[2:9], v[206:213], v[42:45], v187, v188 op_sel_hi:[0,0,0]
	v_mfma_scale_f32_16x16x128_f8f6f4 v[38:41], v[10:17], v[220:227], v[38:41], v187, v188 op_sel_hi:[0,0,0]
	v_mfma_scale_f32_16x16x128_f8f6f4 v[34:37], v[2:9], v[220:227], v[34:37], v187, v188 op_sel_hi:[0,0,0]
	s_setprio 1
	s_barrier
	s_add_i32 s74, 0, 0x18000
	s_add_i32 s75, 0, 0x1c000
	v_add_u32_e32 v14, s74, v183
	v_add_u32_e32 v30, s75, v183
	ds_read_b128 v[2:5], v14
	ds_read_b128 v[6:9], v14 offset:1024
	ds_read_b128 v[10:13], v14 offset:2048
	ds_read_b128 v[14:17], v14 offset:3072
	ds_read_b128 v[18:21], v30
	ds_read_b128 v[22:25], v30 offset:1024
	ds_read_b128 v[26:29], v30 offset:2048
	ds_read_b128 v[30:33], v30 offset:3072
	s_add_u32 s26, s72, 0x40000
	s_addc_u32 s27, s73, 0
	s_mov_b32 m0, s83
	v_lshl_add_u64 v[214:215], s[26:27], 0, v[164:165]
	ds_read_b128 v[190:193], v186 offset:32768
	ds_read_b128 v[194:197], v186 offset:33792
	ds_read_b128 v[198:201], v186 offset:34816
	ds_read_b128 v[202:205], v186 offset:35840
	ds_read_b128 v[206:209], v186 offset:36864
	ds_read_b128 v[210:213], v186 offset:37888
	ds_read_b128 v[220:223], v186 offset:38912
	ds_read_b128 v[224:227], v186 offset:39936
	global_load_lds_dwordx4 v[214:215], off
	v_lshl_add_u64 v[214:215], s[26:27], 0, v[166:167]
	s_mov_b32 m0, s84
	s_nop 0
	global_load_lds_dwordx4 v[214:215], off
	s_waitcnt vmcnt(8)
	s_waitcnt lgkmcnt(0)
	s_barrier
	s_setprio 0
	s_waitcnt lgkmcnt(0)
	v_mfma_scale_f32_16x16x128_f8f6f4 v[158:161], v[2:9], v[190:197], v[158:161], v187, v188 op_sel_hi:[0,0,0]
	v_mfma_scale_f32_16x16x128_f8f6f4 v[154:157], v[10:17], v[190:197], v[154:157], v187, v188 op_sel_hi:[0,0,0]
	v_mfma_scale_f32_16x16x128_f8f6f4 v[150:153], v[2:9], v[198:205], v[150:153], v187, v188 op_sel_hi:[0,0,0]
	v_mfma_scale_f32_16x16x128_f8f6f4 v[142:145], v[10:17], v[198:205], v[142:145], v187, v188 op_sel_hi:[0,0,0]
	v_mfma_scale_f32_16x16x128_f8f6f4 v[134:137], v[2:9], v[206:213], v[134:137], v187, v188 op_sel_hi:[0,0,0]
	v_mfma_scale_f32_16x16x128_f8f6f4 v[126:129], v[10:17], v[206:213], v[126:129], v187, v188 op_sel_hi:[0,0,0]
	v_mfma_scale_f32_16x16x128_f8f6f4 v[118:121], v[2:9], v[220:227], v[118:121], v187, v188 op_sel_hi:[0,0,0]
	v_mfma_scale_f32_16x16x128_f8f6f4 v[110:113], v[10:17], v[220:227], v[110:113], v187, v188 op_sel_hi:[0,0,0]
	v_mfma_scale_f32_16x16x128_f8f6f4 v[146:149], v[18:25], v[190:197], v[146:149], v187, v188 op_sel_hi:[0,0,0]
	v_mfma_scale_f32_16x16x128_f8f6f4 v[138:141], v[26:33], v[190:197], v[138:141], v187, v188 op_sel_hi:[0,0,0]
	v_mfma_scale_f32_16x16x128_f8f6f4 v[130:133], v[18:25], v[198:205], v[130:133], v187, v188 op_sel_hi:[0,0,0]
	v_mfma_scale_f32_16x16x128_f8f6f4 v[122:125], v[26:33], v[198:205], v[122:125], v187, v188 op_sel_hi:[0,0,0]
	v_mfma_scale_f32_16x16x128_f8f6f4 v[114:117], v[18:25], v[206:213], v[114:117], v187, v188 op_sel_hi:[0,0,0]
	v_mfma_scale_f32_16x16x128_f8f6f4 v[106:109], v[26:33], v[206:213], v[106:109], v187, v188 op_sel_hi:[0,0,0]
	v_mfma_scale_f32_16x16x128_f8f6f4 v[102:105], v[18:25], v[220:227], v[102:105], v187, v188 op_sel_hi:[0,0,0]
	v_mfma_scale_f32_16x16x128_f8f6f4 v[98:101], v[26:33], v[220:227], v[98:101], v187, v188 op_sel_hi:[0,0,0]
	s_setprio 1
	s_barrier
	s_add_i32 s26, s74, s80
	v_lshl_add_u64 v[214:215], v[176:177], 0, s[16:17]
	s_mov_b32 m0, s26
	ds_read_b128 v[190:193], v186 offset:49152
	ds_read_b128 v[194:197], v186 offset:50176
	ds_read_b128 v[198:201], v186 offset:51200
	ds_read_b128 v[202:205], v186 offset:52224
	ds_read_b128 v[206:209], v186 offset:53248
	ds_read_b128 v[210:213], v186 offset:54272
	ds_read_b128 v[220:223], v186 offset:55296
	ds_read_b128 v[224:227], v186 offset:56320
	global_load_lds_dwordx4 v[214:215], off
	v_lshl_add_u64 v[214:215], v[176:177], 0, s[18:19]
	s_add_i32 m0, s26, 0x2000
	s_add_i32 s26, s75, s80
	global_load_lds_dwordx4 v[214:215], off
	v_lshl_add_u64 v[214:215], v[176:177], 0, s[22:23]
	s_mov_b32 m0, s26
	v_lshl_add_u64 v[176:177], v[176:177], 0, s[24:25]
	global_load_lds_dwordx4 v[214:215], off
	s_add_i32 m0, s26, 0x2000
	s_nop 0
	global_load_lds_dwordx4 v[176:177], off
	v_lshl_add_u64 v[176:177], v[178:179], 0, s[20:21]
	s_mov_b32 m0, s86
	s_nop 0
	global_load_lds_dwordx4 v[176:177], off
	v_lshl_add_u64 v[176:177], v[180:181], 0, s[20:21]
	s_mov_b32 m0, s87
	s_nop 0
	global_load_lds_dwordx4 v[176:177], off
	s_waitcnt vmcnt(8)
	s_waitcnt lgkmcnt(0)
	s_barrier
	s_setprio 0
	s_waitcnt lgkmcnt(0)
	v_mfma_scale_f32_16x16x128_f8f6f4 v[94:97], v[2:9], v[190:197], v[94:97], v187, v188 op_sel_hi:[0,0,0]
	v_mfma_scale_f32_16x16x128_f8f6f4 v[90:93], v[10:17], v[190:197], v[90:93], v187, v188 op_sel_hi:[0,0,0]
	v_mfma_scale_f32_16x16x128_f8f6f4 v[86:89], v[2:9], v[198:205], v[86:89], v187, v188 op_sel_hi:[0,0,0]
	v_mfma_scale_f32_16x16x128_f8f6f4 v[78:81], v[10:17], v[198:205], v[78:81], v187, v188 op_sel_hi:[0,0,0]
	v_mfma_scale_f32_16x16x128_f8f6f4 v[70:73], v[2:9], v[206:213], v[70:73], v187, v188 op_sel_hi:[0,0,0]
	v_mfma_scale_f32_16x16x128_f8f6f4 v[62:65], v[10:17], v[206:213], v[62:65], v187, v188 op_sel_hi:[0,0,0]
	v_mfma_scale_f32_16x16x128_f8f6f4 v[54:57], v[2:9], v[220:227], v[54:57], v187, v188 op_sel_hi:[0,0,0]
	v_mfma_scale_f32_16x16x128_f8f6f4 v[46:49], v[10:17], v[220:227], v[46:49], v187, v188 op_sel_hi:[0,0,0]
	v_mfma_scale_f32_16x16x128_f8f6f4 v[82:85], v[18:25], v[190:197], v[82:85], v187, v188 op_sel_hi:[0,0,0]
	v_mfma_scale_f32_16x16x128_f8f6f4 v[74:77], v[26:33], v[190:197], v[74:77], v187, v188 op_sel_hi:[0,0,0]
	v_mfma_scale_f32_16x16x128_f8f6f4 v[66:69], v[18:25], v[198:205], v[66:69], v187, v188 op_sel_hi:[0,0,0]
	v_mfma_scale_f32_16x16x128_f8f6f4 v[58:61], v[26:33], v[198:205], v[58:61], v187, v188 op_sel_hi:[0,0,0]
	v_mfma_scale_f32_16x16x128_f8f6f4 v[50:53], v[18:25], v[206:213], v[50:53], v187, v188 op_sel_hi:[0,0,0]
	v_mfma_scale_f32_16x16x128_f8f6f4 v[42:45], v[26:33], v[206:213], v[42:45], v187, v188 op_sel_hi:[0,0,0]
	v_mfma_scale_f32_16x16x128_f8f6f4 v[38:41], v[18:25], v[220:227], v[38:41], v187, v188 op_sel_hi:[0,0,0]
	v_mfma_scale_f32_16x16x128_f8f6f4 v[34:37], v[26:33], v[220:227], v[34:37], v187, v188 op_sel_hi:[0,0,0]
	s_setprio 1
	s_barrier
	s_add_i32 s94, s94, 2
	s_add_u32 s92, s92, 0x10000
	s_addc_u32 s93, s93, 0
	s_add_u32 s70, s70, 0x100
	s_addc_u32 s71, s71, 0
	s_cmp_gt_u32 s94, 13
	s_cbranch_scc0 .LBB0_285
	s_and_b64 vcc, exec, s[40:41]
	s_cbranch_vccz .LBB0_288
	s_barrier

.LBB0_660:
	ds_read_b128 v[130:133], v222
	ds_read_b128 v[134:137], v222 offset:1024
	ds_read_b128 v[138:141], v222 offset:2048
	ds_read_b128 v[142:145], v222 offset:3072
	ds_read_b128 v[146:149], v223
	ds_read_b128 v[150:153], v223 offset:1024
	ds_read_b128 v[154:157], v223 offset:2048
	ds_read_b128 v[158:161], v223 offset:3072
	s_add_u32 s26, s58, 0xfff80080
	s_addc_u32 s27, s59, -1
	s_cmp_eq_u32 s80, 28
	s_cselect_b32 s61, s45, s27
	s_cselect_b32 s60, s72, s26
	s_cselect_b32 s27, s41, s75
	s_cselect_b32 s26, s73, s74
	v_lshl_add_u64 v[208:209], s[58:59], 0, v[200:201]
	s_add_i32 m0, s57, 0xc000
	ds_read_b128 v[162:165], v224
	ds_read_b128 v[166:169], v224 offset:1024
	ds_read_b128 v[170:173], v224 offset:2048
	ds_read_b128 v[174:177], v224 offset:3072
	ds_read_b128 v[178:181], v224 offset:4096
	ds_read_b128 v[182:185], v224 offset:5120
	ds_read_b128 v[186:189], v224 offset:6144
	ds_read_b128 v[190:193], v224 offset:7168
	global_load_lds_dwordx4 v[208:209], off
	v_lshl_add_u64 v[208:209], s[58:59], 0, v[202:203]
	s_add_i32 m0, s57, 0xe000
	s_nop 0
	global_load_lds_dwordx4 v[208:209], off
	s_waitcnt vmcnt(8)
	s_waitcnt lgkmcnt(0)
	s_barrier
	s_setprio 0
	s_waitcnt lgkmcnt(0)
	v_mfma_f32_16x16x32_bf16 v[126:129], v[130:133], v[162:165], v[126:129]
	v_mfma_f32_16x16x32_bf16 v[122:125], v[138:141], v[162:165], v[122:125]
	v_mfma_f32_16x16x32_bf16 v[118:121], v[130:133], v[170:173], v[118:121]
	v_mfma_f32_16x16x32_bf16 v[114:117], v[138:141], v[170:173], v[114:117]
	v_mfma_f32_16x16x32_bf16 v[110:113], v[130:133], v[178:181], v[110:113]
	v_mfma_f32_16x16x32_bf16 v[102:105], v[138:141], v[178:181], v[102:105]
	v_mfma_f32_16x16x32_bf16 v[94:97], v[130:133], v[186:189], v[94:97]
	v_mfma_f32_16x16x32_bf16 v[74:77], v[138:141], v[186:189], v[74:77]
	v_mfma_f32_16x16x32_bf16 v[126:129], v[134:137], v[166:169], v[126:129]
	v_mfma_f32_16x16x32_bf16 v[122:125], v[142:145], v[166:169], v[122:125]
	v_mfma_f32_16x16x32_bf16 v[118:121], v[134:137], v[174:177], v[118:121]
	v_mfma_f32_16x16x32_bf16 v[114:117], v[142:145], v[174:177], v[114:117]
	v_mfma_f32_16x16x32_bf16 v[110:113], v[134:137], v[182:185], v[110:113]
	v_mfma_f32_16x16x32_bf16 v[102:105], v[142:145], v[182:185], v[102:105]
	v_mfma_f32_16x16x32_bf16 v[94:97], v[134:137], v[190:193], v[94:97]
	v_mfma_f32_16x16x32_bf16 v[74:77], v[142:145], v[190:193], v[74:77]
	v_mfma_f32_16x16x32_bf16 v[106:109], v[146:149], v[162:165], v[106:109]
	v_mfma_f32_16x16x32_bf16 v[98:101], v[154:157], v[162:165], v[98:101]
	v_mfma_f32_16x16x32_bf16 v[90:93], v[146:149], v[170:173], v[90:93]
	v_mfma_f32_16x16x32_bf16 v[86:89], v[154:157], v[170:173], v[86:89]
	v_mfma_f32_16x16x32_bf16 v[82:85], v[146:149], v[178:181], v[82:85]
	v_mfma_f32_16x16x32_bf16 v[78:81], v[154:157], v[178:181], v[78:81]
	v_mfma_f32_16x16x32_bf16 v[70:73], v[146:149], v[186:189], v[70:73]
	v_mfma_f32_16x16x32_bf16 v[66:69], v[154:157], v[186:189], v[66:69]
	v_mfma_f32_16x16x32_bf16 v[106:109], v[150:153], v[166:169], v[106:109]
	v_mfma_f32_16x16x32_bf16 v[98:101], v[158:161], v[166:169], v[98:101]
	v_mfma_f32_16x16x32_bf16 v[90:93], v[150:153], v[174:177], v[90:93]
	v_mfma_f32_16x16x32_bf16 v[86:89], v[158:161], v[174:177], v[86:89]
	v_mfma_f32_16x16x32_bf16 v[82:85], v[150:153], v[182:185], v[82:85]
	v_mfma_f32_16x16x32_bf16 v[78:81], v[158:161], v[182:185], v[78:81]
	v_mfma_f32_16x16x32_bf16 v[70:73], v[150:153], v[190:193], v[70:73]
	v_mfma_f32_16x16x32_bf16 v[66:69], v[158:161], v[190:193], v[66:69]
	s_setprio 1
	s_barrier
	v_lshl_add_u64 v[208:209], s[26:27], 0, v[194:195]
	s_add_i32 s26, s70, s35
	s_mov_b32 m0, s26
	ds_read_b128 v[162:165], v224 offset:16384
	ds_read_b128 v[166:169], v224 offset:17408
	ds_read_b128 v[170:173], v224 offset:18432
	ds_read_b128 v[174:177], v224 offset:19456
	ds_read_b128 v[178:181], v224 offset:20480
	ds_read_b128 v[182:185], v224 offset:21504
	ds_read_b128 v[186:189], v224 offset:22528
	ds_read_b128 v[190:193], v224 offset:23552
	global_load_lds_dwordx4 v[208:209], off
	v_lshl_add_u64 v[210:211], v[208:209], 0, s[6:7]
	s_add_i32 m0, s26, 0x2000
	s_add_i32 s26, s71, s35
	global_load_lds_dwordx4 v[210:211], off
	v_lshl_add_u64 v[210:211], v[208:209], 0, s[8:9]
	s_mov_b32 m0, s26
	v_lshl_add_u64 v[212:213], s[60:61], 0, v[198:199]
	global_load_lds_dwordx4 v[210:211], off
	v_lshl_add_u64 v[210:211], v[208:209], 0, s[10:11]
	s_add_i32 m0, s26, 0x2000
	s_nop 0
	global_load_lds_dwordx4 v[210:211], off
	v_lshl_add_u64 v[210:211], s[60:61], 0, v[196:197]
	s_mov_b32 m0, s57
	s_nop 0
	global_load_lds_dwordx4 v[210:211], off
	s_mov_b32 m0, s63
	s_nop 0
	global_load_lds_dwordx4 v[212:213], off
	s_waitcnt vmcnt(8)
	s_waitcnt lgkmcnt(0)
	s_barrier
	s_setprio 0
	s_waitcnt lgkmcnt(0)
	v_mfma_f32_16x16x32_bf16 v[62:65], v[130:133], v[162:165], v[62:65]
	v_mfma_f32_16x16x32_bf16 v[58:61], v[138:141], v[162:165], v[58:61]
	v_mfma_f32_16x16x32_bf16 v[54:57], v[130:133], v[170:173], v[54:57]
	v_mfma_f32_16x16x32_bf16 v[50:53], v[138:141], v[170:173], v[50:53]
	v_mfma_f32_16x16x32_bf16 v[46:49], v[130:133], v[178:181], v[46:49]
	v_mfma_f32_16x16x32_bf16 v[38:41], v[138:141], v[178:181], v[38:41]
	v_mfma_f32_16x16x32_bf16 v[30:33], v[130:133], v[186:189], v[30:33]
	v_mfma_f32_16x16x32_bf16 v[10:13], v[138:141], v[186:189], v[10:13]
	v_mfma_f32_16x16x32_bf16 v[62:65], v[134:137], v[166:169], v[62:65]
	v_mfma_f32_16x16x32_bf16 v[58:61], v[142:145], v[166:169], v[58:61]
	v_mfma_f32_16x16x32_bf16 v[54:57], v[134:137], v[174:177], v[54:57]
	v_mfma_f32_16x16x32_bf16 v[50:53], v[142:145], v[174:177], v[50:53]
	v_mfma_f32_16x16x32_bf16 v[46:49], v[134:137], v[182:185], v[46:49]
	v_mfma_f32_16x16x32_bf16 v[38:41], v[142:145], v[182:185], v[38:41]
	v_mfma_f32_16x16x32_bf16 v[30:33], v[134:137], v[190:193], v[30:33]
	v_mfma_f32_16x16x32_bf16 v[10:13], v[142:145], v[190:193], v[10:13]
	v_mfma_f32_16x16x32_bf16 v[42:45], v[146:149], v[162:165], v[42:45]
	v_mfma_f32_16x16x32_bf16 v[34:37], v[154:157], v[162:165], v[34:37]
	v_mfma_f32_16x16x32_bf16 v[26:29], v[146:149], v[170:173], v[26:29]
	v_mfma_f32_16x16x32_bf16 v[22:25], v[154:157], v[170:173], v[22:25]
	v_mfma_f32_16x16x32_bf16 v[18:21], v[146:149], v[178:181], v[18:21]
	v_mfma_f32_16x16x32_bf16 v[14:17], v[154:157], v[178:181], v[14:17]
	v_mfma_f32_16x16x32_bf16 v[6:9], v[146:149], v[186:189], v[6:9]
	v_mfma_f32_16x16x32_bf16 v[2:5], v[154:157], v[186:189], v[2:5]
	v_mfma_f32_16x16x32_bf16 v[42:45], v[150:153], v[166:169], v[42:45]
	v_mfma_f32_16x16x32_bf16 v[34:37], v[158:161], v[166:169], v[34:37]
	v_mfma_f32_16x16x32_bf16 v[26:29], v[150:153], v[174:177], v[26:29]
	v_mfma_f32_16x16x32_bf16 v[22:25], v[158:161], v[174:177], v[22:25]
	v_mfma_f32_16x16x32_bf16 v[18:21], v[150:153], v[182:185], v[18:21]
	v_mfma_f32_16x16x32_bf16 v[14:17], v[158:161], v[182:185], v[14:17]
	v_mfma_f32_16x16x32_bf16 v[6:9], v[150:153], v[190:193], v[6:9]
	v_mfma_f32_16x16x32_bf16 v[2:5], v[158:161], v[190:193], v[2:5]
	s_setprio 1
	s_barrier
	s_add_i32 s81, 0, 0x18000
	s_add_i32 s82, 0, 0x1c000
	v_add_u32_e32 v142, s81, v220
	v_add_u32_e32 v158, s82, v220
	ds_read_b128 v[130:133], v142
	ds_read_b128 v[134:137], v142 offset:1024
	ds_read_b128 v[138:141], v142 offset:2048
	ds_read_b128 v[142:145], v142 offset:3072
	ds_read_b128 v[146:149], v158
	ds_read_b128 v[150:153], v158 offset:1024
	ds_read_b128 v[154:157], v158 offset:2048
	ds_read_b128 v[158:161], v158 offset:3072
	s_add_u32 s26, s60, 0x80000
	s_addc_u32 s27, s61, 0
	s_mov_b32 m0, s64
	v_lshl_add_u64 v[214:215], s[26:27], 0, v[196:197]
	ds_read_b128 v[162:165], v224 offset:32768
	ds_read_b128 v[166:169], v224 offset:33792
	ds_read_b128 v[170:173], v224 offset:34816
	ds_read_b128 v[174:177], v224 offset:35840
	ds_read_b128 v[178:181], v224 offset:36864
	ds_read_b128 v[182:185], v224 offset:37888
	ds_read_b128 v[186:189], v224 offset:38912
	ds_read_b128 v[190:193], v224 offset:39936
	global_load_lds_dwordx4 v[214:215], off
	v_lshl_add_u64 v[214:215], s[26:27], 0, v[198:199]
	s_mov_b32 m0, s65
	s_nop 0
	global_load_lds_dwordx4 v[214:215], off
	s_waitcnt vmcnt(8)
	s_waitcnt lgkmcnt(0)
	s_barrier
	s_setprio 0
	s_waitcnt lgkmcnt(0)
	v_mfma_f32_16x16x32_bf16 v[126:129], v[130:133], v[162:165], v[126:129]
	v_mfma_f32_16x16x32_bf16 v[122:125], v[138:141], v[162:165], v[122:125]
	v_mfma_f32_16x16x32_bf16 v[118:121], v[130:133], v[170:173], v[118:121]
	v_mfma_f32_16x16x32_bf16 v[114:117], v[138:141], v[170:173], v[114:117]
	v_mfma_f32_16x16x32_bf16 v[110:113], v[130:133], v[178:181], v[110:113]
	v_mfma_f32_16x16x32_bf16 v[102:105], v[138:141], v[178:181], v[102:105]
	v_mfma_f32_16x16x32_bf16 v[94:97], v[130:133], v[186:189], v[94:97]
	v_mfma_f32_16x16x32_bf16 v[74:77], v[138:141], v[186:189], v[74:77]
	v_mfma_f32_16x16x32_bf16 v[126:129], v[134:137], v[166:169], v[126:129]
	v_mfma_f32_16x16x32_bf16 v[122:125], v[142:145], v[166:169], v[122:125]
	v_mfma_f32_16x16x32_bf16 v[118:121], v[134:137], v[174:177], v[118:121]
	v_mfma_f32_16x16x32_bf16 v[114:117], v[142:145], v[174:177], v[114:117]
	v_mfma_f32_16x16x32_bf16 v[110:113], v[134:137], v[182:185], v[110:113]
	v_mfma_f32_16x16x32_bf16 v[102:105], v[142:145], v[182:185], v[102:105]
	v_mfma_f32_16x16x32_bf16 v[94:97], v[134:137], v[190:193], v[94:97]
	v_mfma_f32_16x16x32_bf16 v[74:77], v[142:145], v[190:193], v[74:77]
	v_mfma_f32_16x16x32_bf16 v[106:109], v[146:149], v[162:165], v[106:109]
	v_mfma_f32_16x16x32_bf16 v[98:101], v[154:157], v[162:165], v[98:101]
	v_mfma_f32_16x16x32_bf16 v[90:93], v[146:149], v[170:173], v[90:93]
	v_mfma_f32_16x16x32_bf16 v[86:89], v[154:157], v[170:173], v[86:89]
	v_mfma_f32_16x16x32_bf16 v[82:85], v[146:149], v[178:181], v[82:85]
	v_mfma_f32_16x16x32_bf16 v[78:81], v[154:157], v[178:181], v[78:81]
	v_mfma_f32_16x16x32_bf16 v[70:73], v[146:149], v[186:189], v[70:73]
	v_mfma_f32_16x16x32_bf16 v[66:69], v[154:157], v[186:189], v[66:69]
	v_mfma_f32_16x16x32_bf16 v[106:109], v[150:153], v[166:169], v[106:109]
	v_mfma_f32_16x16x32_bf16 v[98:101], v[158:161], v[166:169], v[98:101]
	v_mfma_f32_16x16x32_bf16 v[90:93], v[150:153], v[174:177], v[90:93]
	v_mfma_f32_16x16x32_bf16 v[86:89], v[158:161], v[174:177], v[86:89]
	v_mfma_f32_16x16x32_bf16 v[82:85], v[150:153], v[182:185], v[82:85]
	v_mfma_f32_16x16x32_bf16 v[78:81], v[158:161], v[182:185], v[78:81]
	v_mfma_f32_16x16x32_bf16 v[70:73], v[150:153], v[190:193], v[70:73]
	v_mfma_f32_16x16x32_bf16 v[66:69], v[158:161], v[190:193], v[66:69]
	s_setprio 1
	s_barrier
	s_add_i32 s26, s81, s35
	v_lshl_add_u64 v[214:215], v[208:209], 0, s[14:15]
	s_mov_b32 m0, s26
	ds_read_b128 v[162:165], v224 offset:49152
	ds_read_b128 v[166:169], v224 offset:50176
	ds_read_b128 v[170:173], v224 offset:51200
	ds_read_b128 v[174:177], v224 offset:52224
	ds_read_b128 v[178:181], v224 offset:53248
	ds_read_b128 v[182:185], v224 offset:54272
	ds_read_b128 v[186:189], v224 offset:55296
	ds_read_b128 v[190:193], v224 offset:56320
	global_load_lds_dwordx4 v[214:215], off
	v_lshl_add_u64 v[214:215], v[208:209], 0, s[16:17]
	s_add_i32 m0, s26, 0x2000
	s_add_i32 s26, s82, s35
	global_load_lds_dwordx4 v[214:215], off
	v_lshl_add_u64 v[214:215], v[208:209], 0, s[20:21]
	s_mov_b32 m0, s26
	v_lshl_add_u64 v[208:209], v[208:209], 0, s[22:23]
	global_load_lds_dwordx4 v[214:215], off
	s_add_i32 m0, s26, 0x2000
	s_nop 0
	global_load_lds_dwordx4 v[208:209], off
	v_lshl_add_u64 v[208:209], v[210:211], 0, s[18:19]
	s_mov_b32 m0, s67
	s_nop 0
	global_load_lds_dwordx4 v[208:209], off
	v_lshl_add_u64 v[208:209], v[212:213], 0, s[18:19]
	s_mov_b32 m0, s68
	s_nop 0
	global_load_lds_dwordx4 v[208:209], off
	s_waitcnt vmcnt(8)
	s_waitcnt lgkmcnt(0)
	s_barrier
	s_setprio 0
	s_waitcnt lgkmcnt(0)
	v_mfma_f32_16x16x32_bf16 v[62:65], v[130:133], v[162:165], v[62:65]
	v_mfma_f32_16x16x32_bf16 v[58:61], v[138:141], v[162:165], v[58:61]
	v_mfma_f32_16x16x32_bf16 v[54:57], v[130:133], v[170:173], v[54:57]
	v_mfma_f32_16x16x32_bf16 v[50:53], v[138:141], v[170:173], v[50:53]
	v_mfma_f32_16x16x32_bf16 v[46:49], v[130:133], v[178:181], v[46:49]
	v_mfma_f32_16x16x32_bf16 v[38:41], v[138:141], v[178:181], v[38:41]
	v_mfma_f32_16x16x32_bf16 v[30:33], v[130:133], v[186:189], v[30:33]
	v_mfma_f32_16x16x32_bf16 v[10:13], v[138:141], v[186:189], v[10:13]
	v_mfma_f32_16x16x32_bf16 v[62:65], v[134:137], v[166:169], v[62:65]
	v_mfma_f32_16x16x32_bf16 v[58:61], v[142:145], v[166:169], v[58:61]
	v_mfma_f32_16x16x32_bf16 v[54:57], v[134:137], v[174:177], v[54:57]
	v_mfma_f32_16x16x32_bf16 v[50:53], v[142:145], v[174:177], v[50:53]
	v_mfma_f32_16x16x32_bf16 v[46:49], v[134:137], v[182:185], v[46:49]
	v_mfma_f32_16x16x32_bf16 v[38:41], v[142:145], v[182:185], v[38:41]
	v_mfma_f32_16x16x32_bf16 v[30:33], v[134:137], v[190:193], v[30:33]
	v_mfma_f32_16x16x32_bf16 v[10:13], v[142:145], v[190:193], v[10:13]
	v_mfma_f32_16x16x32_bf16 v[42:45], v[146:149], v[162:165], v[42:45]
	v_mfma_f32_16x16x32_bf16 v[34:37], v[154:157], v[162:165], v[34:37]
	v_mfma_f32_16x16x32_bf16 v[26:29], v[146:149], v[170:173], v[26:29]
	v_mfma_f32_16x16x32_bf16 v[22:25], v[154:157], v[170:173], v[22:25]
	v_mfma_f32_16x16x32_bf16 v[18:21], v[146:149], v[178:181], v[18:21]
	v_mfma_f32_16x16x32_bf16 v[14:17], v[154:157], v[178:181], v[14:17]
	v_mfma_f32_16x16x32_bf16 v[6:9], v[146:149], v[186:189], v[6:9]
	v_mfma_f32_16x16x32_bf16 v[2:5], v[154:157], v[186:189], v[2:5]
	v_mfma_f32_16x16x32_bf16 v[42:45], v[150:153], v[166:169], v[42:45]
	v_mfma_f32_16x16x32_bf16 v[34:37], v[158:161], v[166:169], v[34:37]
	v_mfma_f32_16x16x32_bf16 v[26:29], v[150:153], v[174:177], v[26:29]
	v_mfma_f32_16x16x32_bf16 v[22:25], v[158:161], v[174:177], v[22:25]
	v_mfma_f32_16x16x32_bf16 v[18:21], v[150:153], v[182:185], v[18:21]
	v_mfma_f32_16x16x32_bf16 v[14:17], v[158:161], v[182:185], v[14:17]
	v_mfma_f32_16x16x32_bf16 v[6:9], v[150:153], v[190:193], v[6:9]
	v_mfma_f32_16x16x32_bf16 v[2:5], v[158:161], v[190:193], v[2:5]
	s_setprio 1
	s_barrier
	s_add_i32 s80, s80, 2
	s_add_u32 s74, s74, 0x10000
	s_addc_u32 s75, s75, 0
	s_add_u32 s58, s58, 0x100
	s_addc_u32 s59, s59, 0
	s_cmp_gt_u32 s80, 29
	s_cbranch_scc0 .LBB0_660
	s_and_b64 vcc, exec, s[24:25]
	s_cbranch_vccz .LBB0_663
	s_barrier

.LBB0_783:
	ds_read_b128 v[144:147], v151
	ds_read_b128 v[156:159], v151 offset:1024
	ds_read_b128 v[160:163], v151 offset:2048
	ds_read_b128 v[164:167], v151 offset:3072
	ds_read_b128 v[168:171], v152
	ds_read_b128 v[172:175], v152 offset:1024
	ds_read_b128 v[176:179], v152 offset:2048
	ds_read_b128 v[180:183], v152 offset:3072
	s_add_u32 s26, s62, 0xfff80080
	s_addc_u32 s27, s63, -1
	s_cmp_eq_u32 s85, 28
	s_cselect_b32 s65, s55, s27
	s_cselect_b32 s64, s81, s26
	s_cselect_b32 s27, s53, s84
	s_cselect_b32 s26, s82, s83
	v_lshl_add_u64 v[216:217], s[62:63], 0, v[136:137]
	s_add_i32 m0, s61, 0xc000
	ds_read_b128 v[184:187], v153
	ds_read_b128 v[188:191], v153 offset:1024
	ds_read_b128 v[192:195], v153 offset:2048
	ds_read_b128 v[196:199], v153 offset:3072
	ds_read_b128 v[200:203], v153 offset:4096
	ds_read_b128 v[204:207], v153 offset:5120
	ds_read_b128 v[208:211], v153 offset:6144
	ds_read_b128 v[212:215], v153 offset:7168
	global_load_lds_dwordx4 v[216:217], off
	v_lshl_add_u64 v[216:217], s[62:63], 0, v[138:139]
	s_add_i32 m0, s61, 0xe000
	s_nop 0
	global_load_lds_dwordx4 v[216:217], off
	s_waitcnt vmcnt(8)
	s_waitcnt lgkmcnt(0)
	s_barrier
	s_setprio 0
	s_waitcnt lgkmcnt(0)
	v_mfma_f32_16x16x32_bf16 v[126:129], v[144:147], v[184:187], v[126:129]
	v_mfma_f32_16x16x32_bf16 v[118:121], v[160:163], v[184:187], v[118:121]
	v_mfma_f32_16x16x32_bf16 v[110:113], v[144:147], v[192:195], v[110:113]
	v_mfma_f32_16x16x32_bf16 v[102:105], v[160:163], v[192:195], v[102:105]
	v_mfma_f32_16x16x32_bf16 v[94:97], v[144:147], v[200:203], v[94:97]
	v_mfma_f32_16x16x32_bf16 v[86:89], v[160:163], v[200:203], v[86:89]
	v_mfma_f32_16x16x32_bf16 v[78:81], v[144:147], v[208:211], v[78:81]
	v_mfma_f32_16x16x32_bf16 v[70:73], v[160:163], v[208:211], v[70:73]
	v_mfma_f32_16x16x32_bf16 v[126:129], v[156:159], v[188:191], v[126:129]
	v_mfma_f32_16x16x32_bf16 v[118:121], v[164:167], v[188:191], v[118:121]
	v_mfma_f32_16x16x32_bf16 v[110:113], v[156:159], v[196:199], v[110:113]
	v_mfma_f32_16x16x32_bf16 v[102:105], v[164:167], v[196:199], v[102:105]
	v_mfma_f32_16x16x32_bf16 v[94:97], v[156:159], v[204:207], v[94:97]
	v_mfma_f32_16x16x32_bf16 v[86:89], v[164:167], v[204:207], v[86:89]
	v_mfma_f32_16x16x32_bf16 v[78:81], v[156:159], v[212:215], v[78:81]
	v_mfma_f32_16x16x32_bf16 v[70:73], v[164:167], v[212:215], v[70:73]
	v_mfma_f32_16x16x32_bf16 v[122:125], v[168:171], v[184:187], v[122:125]
	v_mfma_f32_16x16x32_bf16 v[114:117], v[176:179], v[184:187], v[114:117]
	v_mfma_f32_16x16x32_bf16 v[106:109], v[168:171], v[192:195], v[106:109]
	v_mfma_f32_16x16x32_bf16 v[98:101], v[176:179], v[192:195], v[98:101]
	v_mfma_f32_16x16x32_bf16 v[90:93], v[168:171], v[200:203], v[90:93]
	v_mfma_f32_16x16x32_bf16 v[82:85], v[176:179], v[200:203], v[82:85]
	v_mfma_f32_16x16x32_bf16 v[74:77], v[168:171], v[208:211], v[74:77]
	v_mfma_f32_16x16x32_bf16 v[66:69], v[176:179], v[208:211], v[66:69]
	v_mfma_f32_16x16x32_bf16 v[122:125], v[172:175], v[188:191], v[122:125]
	v_mfma_f32_16x16x32_bf16 v[114:117], v[180:183], v[188:191], v[114:117]
	v_mfma_f32_16x16x32_bf16 v[106:109], v[172:175], v[196:199], v[106:109]
	v_mfma_f32_16x16x32_bf16 v[98:101], v[180:183], v[196:199], v[98:101]
	v_mfma_f32_16x16x32_bf16 v[90:93], v[172:175], v[204:207], v[90:93]
	v_mfma_f32_16x16x32_bf16 v[82:85], v[180:183], v[204:207], v[82:85]
	v_mfma_f32_16x16x32_bf16 v[74:77], v[172:175], v[212:215], v[74:77]
	v_mfma_f32_16x16x32_bf16 v[66:69], v[180:183], v[212:215], v[66:69]
	s_setprio 1
	s_barrier
	v_lshl_add_u64 v[216:217], s[26:27], 0, v[130:131]
	s_add_i32 s26, s73, s35
	s_mov_b32 m0, s26
	ds_read_b128 v[184:187], v153 offset:16384
	ds_read_b128 v[188:191], v153 offset:17408
	ds_read_b128 v[192:195], v153 offset:18432
	ds_read_b128 v[196:199], v153 offset:19456
	ds_read_b128 v[200:203], v153 offset:20480
	ds_read_b128 v[204:207], v153 offset:21504
	ds_read_b128 v[208:211], v153 offset:22528
	ds_read_b128 v[212:215], v153 offset:23552
	global_load_lds_dwordx4 v[216:217], off
	v_lshl_add_u64 v[220:221], v[216:217], 0, s[6:7]
	s_add_i32 m0, s26, 0x2000
	s_add_i32 s26, s74, s35
	global_load_lds_dwordx4 v[220:221], off
	v_lshl_add_u64 v[220:221], v[216:217], 0, s[8:9]
	s_mov_b32 m0, s26
	v_lshl_add_u64 v[222:223], s[64:65], 0, v[134:135]
	global_load_lds_dwordx4 v[220:221], off
	v_lshl_add_u64 v[220:221], v[216:217], 0, s[10:11]
	s_add_i32 m0, s26, 0x2000
	s_nop 0
	global_load_lds_dwordx4 v[220:221], off
	v_lshl_add_u64 v[220:221], s[64:65], 0, v[132:133]
	s_mov_b32 m0, s61
	s_nop 0
	global_load_lds_dwordx4 v[220:221], off
	s_mov_b32 m0, s66
	s_nop 0
	global_load_lds_dwordx4 v[222:223], off
	s_waitcnt vmcnt(8)
	s_waitcnt lgkmcnt(0)
	s_barrier
	s_setprio 0
	s_waitcnt lgkmcnt(0)
	v_mfma_f32_16x16x32_bf16 v[62:65], v[144:147], v[184:187], v[62:65]
	v_mfma_f32_16x16x32_bf16 v[54:57], v[160:163], v[184:187], v[54:57]
	v_mfma_f32_16x16x32_bf16 v[46:49], v[144:147], v[192:195], v[46:49]
	v_mfma_f32_16x16x32_bf16 v[38:41], v[160:163], v[192:195], v[38:41]
	v_mfma_f32_16x16x32_bf16 v[30:33], v[144:147], v[200:203], v[30:33]
	v_mfma_f32_16x16x32_bf16 v[22:25], v[160:163], v[200:203], v[22:25]
	v_mfma_f32_16x16x32_bf16 v[14:17], v[144:147], v[208:211], v[14:17]
	v_mfma_f32_16x16x32_bf16 v[6:9], v[160:163], v[208:211], v[6:9]
	v_mfma_f32_16x16x32_bf16 v[62:65], v[156:159], v[188:191], v[62:65]
	v_mfma_f32_16x16x32_bf16 v[54:57], v[164:167], v[188:191], v[54:57]
	v_mfma_f32_16x16x32_bf16 v[46:49], v[156:159], v[196:199], v[46:49]
	v_mfma_f32_16x16x32_bf16 v[38:41], v[164:167], v[196:199], v[38:41]
	v_mfma_f32_16x16x32_bf16 v[30:33], v[156:159], v[204:207], v[30:33]
	v_mfma_f32_16x16x32_bf16 v[22:25], v[164:167], v[204:207], v[22:25]
	v_mfma_f32_16x16x32_bf16 v[14:17], v[156:159], v[212:215], v[14:17]
	v_mfma_f32_16x16x32_bf16 v[6:9], v[164:167], v[212:215], v[6:9]
	v_mfma_f32_16x16x32_bf16 v[58:61], v[168:171], v[184:187], v[58:61]
	v_mfma_f32_16x16x32_bf16 v[50:53], v[176:179], v[184:187], v[50:53]
	v_mfma_f32_16x16x32_bf16 v[42:45], v[168:171], v[192:195], v[42:45]
	v_mfma_f32_16x16x32_bf16 v[34:37], v[176:179], v[192:195], v[34:37]
	v_mfma_f32_16x16x32_bf16 v[26:29], v[168:171], v[200:203], v[26:29]
	v_mfma_f32_16x16x32_bf16 v[18:21], v[176:179], v[200:203], v[18:21]
	v_mfma_f32_16x16x32_bf16 v[10:13], v[168:171], v[208:211], v[10:13]
	v_mfma_f32_16x16x32_bf16 v[2:5], v[176:179], v[208:211], v[2:5]
	v_mfma_f32_16x16x32_bf16 v[58:61], v[172:175], v[188:191], v[58:61]
	v_mfma_f32_16x16x32_bf16 v[50:53], v[180:183], v[188:191], v[50:53]
	v_mfma_f32_16x16x32_bf16 v[42:45], v[172:175], v[196:199], v[42:45]
	v_mfma_f32_16x16x32_bf16 v[34:37], v[180:183], v[196:199], v[34:37]
	v_mfma_f32_16x16x32_bf16 v[26:29], v[172:175], v[204:207], v[26:29]
	v_mfma_f32_16x16x32_bf16 v[18:21], v[180:183], v[204:207], v[18:21]
	v_mfma_f32_16x16x32_bf16 v[10:13], v[172:175], v[212:215], v[10:13]
	v_mfma_f32_16x16x32_bf16 v[2:5], v[180:183], v[212:215], v[2:5]
	s_setprio 1
	s_barrier
	s_add_i32 s86, 0, 0x18000
	v_add_u32_e32 v155, s86, v149
	s_add_i32 s87, 0, 0x1c000
	ds_read_b128 v[144:147], v155
	ds_read_b128 v[156:159], v155 offset:1024
	ds_read_b128 v[160:163], v155 offset:2048
	ds_read_b128 v[164:167], v155 offset:3072
	v_add_u32_e32 v155, s87, v149
	ds_read_b128 v[168:171], v155
	ds_read_b128 v[172:175], v155 offset:1024
	ds_read_b128 v[176:179], v155 offset:2048
	ds_read_b128 v[180:183], v155 offset:3072
	s_add_u32 s26, s64, 0x80000
	s_addc_u32 s27, s65, 0
	s_mov_b32 m0, s67
	v_lshl_add_u64 v[224:225], s[26:27], 0, v[132:133]
	ds_read_b128 v[184:187], v153 offset:32768
	ds_read_b128 v[188:191], v153 offset:33792
	ds_read_b128 v[192:195], v153 offset:34816
	ds_read_b128 v[196:199], v153 offset:35840
	ds_read_b128 v[200:203], v153 offset:36864
	ds_read_b128 v[204:207], v153 offset:37888
	ds_read_b128 v[208:211], v153 offset:38912
	ds_read_b128 v[212:215], v153 offset:39936
	global_load_lds_dwordx4 v[224:225], off
	v_lshl_add_u64 v[224:225], s[26:27], 0, v[134:135]
	s_mov_b32 m0, s68
	s_nop 0
	global_load_lds_dwordx4 v[224:225], off
	s_waitcnt vmcnt(8)
	s_waitcnt lgkmcnt(0)
	s_barrier
	s_setprio 0
	s_waitcnt lgkmcnt(0)
	v_mfma_f32_16x16x32_bf16 v[126:129], v[144:147], v[184:187], v[126:129]
	v_mfma_f32_16x16x32_bf16 v[118:121], v[160:163], v[184:187], v[118:121]
	v_mfma_f32_16x16x32_bf16 v[110:113], v[144:147], v[192:195], v[110:113]
	v_mfma_f32_16x16x32_bf16 v[102:105], v[160:163], v[192:195], v[102:105]
	v_mfma_f32_16x16x32_bf16 v[94:97], v[144:147], v[200:203], v[94:97]
	v_mfma_f32_16x16x32_bf16 v[86:89], v[160:163], v[200:203], v[86:89]
	v_mfma_f32_16x16x32_bf16 v[78:81], v[144:147], v[208:211], v[78:81]
	v_mfma_f32_16x16x32_bf16 v[70:73], v[160:163], v[208:211], v[70:73]
	v_mfma_f32_16x16x32_bf16 v[126:129], v[156:159], v[188:191], v[126:129]
	v_mfma_f32_16x16x32_bf16 v[118:121], v[164:167], v[188:191], v[118:121]
	v_mfma_f32_16x16x32_bf16 v[110:113], v[156:159], v[196:199], v[110:113]
	v_mfma_f32_16x16x32_bf16 v[102:105], v[164:167], v[196:199], v[102:105]
	v_mfma_f32_16x16x32_bf16 v[94:97], v[156:159], v[204:207], v[94:97]
	v_mfma_f32_16x16x32_bf16 v[86:89], v[164:167], v[204:207], v[86:89]
	v_mfma_f32_16x16x32_bf16 v[78:81], v[156:159], v[212:215], v[78:81]
	v_mfma_f32_16x16x32_bf16 v[70:73], v[164:167], v[212:215], v[70:73]
	v_mfma_f32_16x16x32_bf16 v[122:125], v[168:171], v[184:187], v[122:125]
	v_mfma_f32_16x16x32_bf16 v[114:117], v[176:179], v[184:187], v[114:117]
	v_mfma_f32_16x16x32_bf16 v[106:109], v[168:171], v[192:195], v[106:109]
	v_mfma_f32_16x16x32_bf16 v[98:101], v[176:179], v[192:195], v[98:101]
	v_mfma_f32_16x16x32_bf16 v[90:93], v[168:171], v[200:203], v[90:93]
	v_mfma_f32_16x16x32_bf16 v[82:85], v[176:179], v[200:203], v[82:85]
	v_mfma_f32_16x16x32_bf16 v[74:77], v[168:171], v[208:211], v[74:77]
	v_mfma_f32_16x16x32_bf16 v[66:69], v[176:179], v[208:211], v[66:69]
	v_mfma_f32_16x16x32_bf16 v[122:125], v[172:175], v[188:191], v[122:125]
	v_mfma_f32_16x16x32_bf16 v[114:117], v[180:183], v[188:191], v[114:117]
	v_mfma_f32_16x16x32_bf16 v[106:109], v[172:175], v[196:199], v[106:109]
	v_mfma_f32_16x16x32_bf16 v[98:101], v[180:183], v[196:199], v[98:101]
	v_mfma_f32_16x16x32_bf16 v[90:93], v[172:175], v[204:207], v[90:93]
	v_mfma_f32_16x16x32_bf16 v[82:85], v[180:183], v[204:207], v[82:85]
	v_mfma_f32_16x16x32_bf16 v[74:77], v[172:175], v[212:215], v[74:77]
	v_mfma_f32_16x16x32_bf16 v[66:69], v[180:183], v[212:215], v[66:69]
	s_setprio 1
	s_barrier
	s_add_i32 s26, s86, s35
	v_lshl_add_u64 v[224:225], v[216:217], 0, s[16:17]
	s_mov_b32 m0, s26
	ds_read_b128 v[184:187], v153 offset:49152
	ds_read_b128 v[188:191], v153 offset:50176
	ds_read_b128 v[192:195], v153 offset:51200
	ds_read_b128 v[196:199], v153 offset:52224
	ds_read_b128 v[200:203], v153 offset:53248
	ds_read_b128 v[204:207], v153 offset:54272
	ds_read_b128 v[208:211], v153 offset:55296
	ds_read_b128 v[212:215], v153 offset:56320
	global_load_lds_dwordx4 v[224:225], off
	v_lshl_add_u64 v[224:225], v[216:217], 0, s[18:19]
	s_add_i32 m0, s26, 0x2000
	s_add_i32 s26, s87, s35
	global_load_lds_dwordx4 v[224:225], off
	v_lshl_add_u64 v[224:225], v[216:217], 0, s[22:23]
	s_mov_b32 m0, s26
	v_lshl_add_u64 v[216:217], v[216:217], 0, s[24:25]
	global_load_lds_dwordx4 v[224:225], off
	s_add_i32 m0, s26, 0x2000
	s_nop 0
	global_load_lds_dwordx4 v[216:217], off
	v_lshl_add_u64 v[216:217], v[220:221], 0, s[20:21]
	s_mov_b32 m0, s70
	s_nop 0
	global_load_lds_dwordx4 v[216:217], off
	v_lshl_add_u64 v[216:217], v[222:223], 0, s[20:21]
	s_mov_b32 m0, s71
	s_nop 0
	global_load_lds_dwordx4 v[216:217], off
	s_waitcnt vmcnt(8)
	s_waitcnt lgkmcnt(0)
	s_barrier
	s_setprio 0
	s_waitcnt lgkmcnt(0)
	v_mfma_f32_16x16x32_bf16 v[62:65], v[144:147], v[184:187], v[62:65]
	v_mfma_f32_16x16x32_bf16 v[54:57], v[160:163], v[184:187], v[54:57]
	v_mfma_f32_16x16x32_bf16 v[46:49], v[144:147], v[192:195], v[46:49]
	v_mfma_f32_16x16x32_bf16 v[38:41], v[160:163], v[192:195], v[38:41]
	v_mfma_f32_16x16x32_bf16 v[30:33], v[144:147], v[200:203], v[30:33]
	v_mfma_f32_16x16x32_bf16 v[22:25], v[160:163], v[200:203], v[22:25]
	v_mfma_f32_16x16x32_bf16 v[14:17], v[144:147], v[208:211], v[14:17]
	v_mfma_f32_16x16x32_bf16 v[6:9], v[160:163], v[208:211], v[6:9]
	v_mfma_f32_16x16x32_bf16 v[62:65], v[156:159], v[188:191], v[62:65]
	v_mfma_f32_16x16x32_bf16 v[54:57], v[164:167], v[188:191], v[54:57]
	v_mfma_f32_16x16x32_bf16 v[46:49], v[156:159], v[196:199], v[46:49]
	v_mfma_f32_16x16x32_bf16 v[38:41], v[164:167], v[196:199], v[38:41]
	v_mfma_f32_16x16x32_bf16 v[30:33], v[156:159], v[204:207], v[30:33]
	v_mfma_f32_16x16x32_bf16 v[22:25], v[164:167], v[204:207], v[22:25]
	v_mfma_f32_16x16x32_bf16 v[14:17], v[156:159], v[212:215], v[14:17]
	v_mfma_f32_16x16x32_bf16 v[6:9], v[164:167], v[212:215], v[6:9]
	v_mfma_f32_16x16x32_bf16 v[58:61], v[168:171], v[184:187], v[58:61]
	v_mfma_f32_16x16x32_bf16 v[50:53], v[176:179], v[184:187], v[50:53]
	v_mfma_f32_16x16x32_bf16 v[42:45], v[168:171], v[192:195], v[42:45]
	v_mfma_f32_16x16x32_bf16 v[34:37], v[176:179], v[192:195], v[34:37]
	v_mfma_f32_16x16x32_bf16 v[26:29], v[168:171], v[200:203], v[26:29]
	v_mfma_f32_16x16x32_bf16 v[18:21], v[176:179], v[200:203], v[18:21]
	v_mfma_f32_16x16x32_bf16 v[10:13], v[168:171], v[208:211], v[10:13]
	v_mfma_f32_16x16x32_bf16 v[2:5], v[176:179], v[208:211], v[2:5]
	v_mfma_f32_16x16x32_bf16 v[58:61], v[172:175], v[188:191], v[58:61]
	v_mfma_f32_16x16x32_bf16 v[50:53], v[180:183], v[188:191], v[50:53]
	v_mfma_f32_16x16x32_bf16 v[42:45], v[172:175], v[196:199], v[42:45]
	v_mfma_f32_16x16x32_bf16 v[34:37], v[180:183], v[196:199], v[34:37]
	v_mfma_f32_16x16x32_bf16 v[26:29], v[172:175], v[204:207], v[26:29]
	v_mfma_f32_16x16x32_bf16 v[18:21], v[180:183], v[204:207], v[18:21]
	v_mfma_f32_16x16x32_bf16 v[10:13], v[172:175], v[212:215], v[10:13]
	v_mfma_f32_16x16x32_bf16 v[2:5], v[180:183], v[212:215], v[2:5]
	s_setprio 1
	s_barrier
	s_add_i32 s85, s85, 2
	s_add_u32 s83, s83, 0x10000
	s_addc_u32 s84, s84, 0
	s_add_u32 s62, s62, 0x100
	s_addc_u32 s63, s63, 0
	s_cmp_gt_u32 s85, 29
	s_cbranch_scc0 .LBB0_783
	s_and_b64 vcc, exec, s[40:41]
	s_cbranch_vccz .LBB0_786
	s_barrier

.LBB0_858:
	ds_read_b128 v[26:29], v185
	ds_read_b128 v[30:33], v185 offset:1024
	ds_read_b128 v[18:21], v185 offset:2048
	ds_read_b128 v[22:25], v185 offset:3072
	ds_read_b128 v[10:13], v186
	ds_read_b128 v[14:17], v186 offset:1024
	ds_read_b128 v[2:5], v186 offset:2048
	ds_read_b128 v[6:9], v186 offset:3072
	s_add_u32 s26, s50, 0xfff50080
	s_addc_u32 s27, s51, -1
	s_cmp_eq_u32 s74, 40
	s_cselect_b32 s53, s5, s27
	s_cselect_b32 s52, s4, s26
	s_cselect_b32 s55, s45, s73
	s_cselect_b32 s54, s44, s72
	v_lshl_add_u64 v[176:177], s[50:51], 0, v[168:169]
	s_add_i32 m0, s59, 0xc000
	ds_read_b128 v[190:193], v187
	ds_read_b128 v[194:197], v187 offset:1024
	ds_read_b128 v[198:201], v187 offset:2048
	ds_read_b128 v[202:205], v187 offset:3072
	ds_read_b128 v[206:209], v187 offset:4096
	ds_read_b128 v[210:213], v187 offset:5120
	ds_read_b128 v[220:223], v187 offset:6144
	ds_read_b128 v[224:227], v187 offset:7168
	global_load_lds_dwordx4 v[176:177], off
	v_lshl_add_u64 v[176:177], s[50:51], 0, v[170:171]
	s_add_i32 m0, s59, 0xe000
	s_nop 0
	global_load_lds_dwordx4 v[176:177], off
	s_waitcnt vmcnt(8)
	s_waitcnt lgkmcnt(0)
	s_barrier
	s_setprio 0
	s_waitcnt lgkmcnt(0)
	v_mfma_scale_f32_16x16x128_f8f6f4 v[158:161], v[26:33], v[190:197], v[158:161], v188, v189 op_sel_hi:[0,0,0]
	v_mfma_scale_f32_16x16x128_f8f6f4 v[154:157], v[18:25], v[190:197], v[154:157], v188, v189 op_sel_hi:[0,0,0]
	v_mfma_scale_f32_16x16x128_f8f6f4 v[150:153], v[26:33], v[198:205], v[150:153], v188, v189 op_sel_hi:[0,0,0]
	v_mfma_scale_f32_16x16x128_f8f6f4 v[146:149], v[18:25], v[198:205], v[146:149], v188, v189 op_sel_hi:[0,0,0]
	v_mfma_scale_f32_16x16x128_f8f6f4 v[138:141], v[26:33], v[206:213], v[138:141], v188, v189 op_sel_hi:[0,0,0]
	v_mfma_scale_f32_16x16x128_f8f6f4 v[130:133], v[18:25], v[206:213], v[130:133], v188, v189 op_sel_hi:[0,0,0]
	v_mfma_scale_f32_16x16x128_f8f6f4 v[122:125], v[26:33], v[220:227], v[122:125], v188, v189 op_sel_hi:[0,0,0]
	v_mfma_scale_f32_16x16x128_f8f6f4 v[114:117], v[18:25], v[220:227], v[114:117], v188, v189 op_sel_hi:[0,0,0]
	v_mfma_scale_f32_16x16x128_f8f6f4 v[142:145], v[10:17], v[190:197], v[142:145], v188, v189 op_sel_hi:[0,0,0]
	v_mfma_scale_f32_16x16x128_f8f6f4 v[134:137], v[2:9], v[190:197], v[134:137], v188, v189 op_sel_hi:[0,0,0]
	v_mfma_scale_f32_16x16x128_f8f6f4 v[126:129], v[10:17], v[198:205], v[126:129], v188, v189 op_sel_hi:[0,0,0]
	v_mfma_scale_f32_16x16x128_f8f6f4 v[118:121], v[2:9], v[198:205], v[118:121], v188, v189 op_sel_hi:[0,0,0]
	v_mfma_scale_f32_16x16x128_f8f6f4 v[110:113], v[10:17], v[206:213], v[110:113], v188, v189 op_sel_hi:[0,0,0]
	v_mfma_scale_f32_16x16x128_f8f6f4 v[106:109], v[2:9], v[206:213], v[106:109], v188, v189 op_sel_hi:[0,0,0]
	v_mfma_scale_f32_16x16x128_f8f6f4 v[102:105], v[10:17], v[220:227], v[102:105], v188, v189 op_sel_hi:[0,0,0]
	v_mfma_scale_f32_16x16x128_f8f6f4 v[98:101], v[2:9], v[220:227], v[98:101], v188, v189 op_sel_hi:[0,0,0]
	s_setprio 1
	s_barrier
	s_add_i32 s26, s67, s57
	v_lshl_add_u64 v[176:177], s[54:55], 0, v[162:163]
	s_mov_b32 m0, s26
	ds_read_b128 v[190:193], v187 offset:16384
	ds_read_b128 v[194:197], v187 offset:17408
	ds_read_b128 v[198:201], v187 offset:18432
	ds_read_b128 v[202:205], v187 offset:19456
	ds_read_b128 v[206:209], v187 offset:20480
	ds_read_b128 v[210:213], v187 offset:21504
	ds_read_b128 v[220:223], v187 offset:22528
	ds_read_b128 v[224:227], v187 offset:23552
	global_load_lds_dwordx4 v[176:177], off
	v_lshl_add_u64 v[178:179], v[176:177], 0, s[8:9]
	s_add_i32 m0, s26, 0x2000
	s_add_i32 s26, s68, s57
	global_load_lds_dwordx4 v[178:179], off
	v_lshl_add_u64 v[178:179], v[176:177], 0, s[10:11]
	s_mov_b32 m0, s26
	v_lshl_add_u64 v[180:181], s[52:53], 0, v[166:167]
	global_load_lds_dwordx4 v[178:179], off
	v_lshl_add_u64 v[178:179], v[176:177], 0, s[12:13]
	s_add_i32 m0, s26, 0x2000
	s_nop 0
	global_load_lds_dwordx4 v[178:179], off
	v_lshl_add_u64 v[178:179], s[52:53], 0, v[164:165]
	s_mov_b32 m0, s59
	s_nop 0
	global_load_lds_dwordx4 v[178:179], off
	s_mov_b32 m0, s60
	s_nop 0
	global_load_lds_dwordx4 v[180:181], off
	s_waitcnt vmcnt(8)
	s_waitcnt lgkmcnt(0)
	s_barrier
	s_setprio 0
	s_waitcnt lgkmcnt(0)
	v_mfma_scale_f32_16x16x128_f8f6f4 v[94:97], v[26:33], v[190:197], v[94:97], v188, v189 op_sel_hi:[0,0,0]
	v_mfma_scale_f32_16x16x128_f8f6f4 v[90:93], v[18:25], v[190:197], v[90:93], v188, v189 op_sel_hi:[0,0,0]
	v_mfma_scale_f32_16x16x128_f8f6f4 v[86:89], v[26:33], v[198:205], v[86:89], v188, v189 op_sel_hi:[0,0,0]
	v_mfma_scale_f32_16x16x128_f8f6f4 v[78:81], v[18:25], v[198:205], v[78:81], v188, v189 op_sel_hi:[0,0,0]
	v_mfma_scale_f32_16x16x128_f8f6f4 v[70:73], v[26:33], v[206:213], v[70:73], v188, v189 op_sel_hi:[0,0,0]
	v_mfma_scale_f32_16x16x128_f8f6f4 v[62:65], v[18:25], v[206:213], v[62:65], v188, v189 op_sel_hi:[0,0,0]
	v_mfma_scale_f32_16x16x128_f8f6f4 v[54:57], v[26:33], v[220:227], v[54:57], v188, v189 op_sel_hi:[0,0,0]
	v_mfma_scale_f32_16x16x128_f8f6f4 v[46:49], v[18:25], v[220:227], v[46:49], v188, v189 op_sel_hi:[0,0,0]
	v_mfma_scale_f32_16x16x128_f8f6f4 v[82:85], v[10:17], v[190:197], v[82:85], v188, v189 op_sel_hi:[0,0,0]
	v_mfma_scale_f32_16x16x128_f8f6f4 v[74:77], v[2:9], v[190:197], v[74:77], v188, v189 op_sel_hi:[0,0,0]
	v_mfma_scale_f32_16x16x128_f8f6f4 v[66:69], v[10:17], v[198:205], v[66:69], v188, v189 op_sel_hi:[0,0,0]
	v_mfma_scale_f32_16x16x128_f8f6f4 v[58:61], v[2:9], v[198:205], v[58:61], v188, v189 op_sel_hi:[0,0,0]
	v_mfma_scale_f32_16x16x128_f8f6f4 v[50:53], v[10:17], v[206:213], v[50:53], v188, v189 op_sel_hi:[0,0,0]
	v_mfma_scale_f32_16x16x128_f8f6f4 v[42:45], v[2:9], v[206:213], v[42:45], v188, v189 op_sel_hi:[0,0,0]
	v_mfma_scale_f32_16x16x128_f8f6f4 v[38:41], v[10:17], v[220:227], v[38:41], v188, v189 op_sel_hi:[0,0,0]
	v_mfma_scale_f32_16x16x128_f8f6f4 v[34:37], v[2:9], v[220:227], v[34:37], v188, v189 op_sel_hi:[0,0,0]
	s_setprio 1
	s_barrier
	s_add_i32 s54, 0, 0x18000
	s_add_i32 s55, 0, 0x1c000
	v_add_u32_e32 v14, s54, v183
	v_add_u32_e32 v30, s55, v183
	ds_read_b128 v[2:5], v14
	ds_read_b128 v[6:9], v14 offset:1024
	ds_read_b128 v[10:13], v14 offset:2048
	ds_read_b128 v[14:17], v14 offset:3072
	ds_read_b128 v[18:21], v30
	ds_read_b128 v[22:25], v30 offset:1024
	ds_read_b128 v[26:29], v30 offset:2048
	ds_read_b128 v[30:33], v30 offset:3072
	s_add_u32 s26, s52, 0xb0000
	s_addc_u32 s27, s53, 0
	s_mov_b32 m0, s61
	v_lshl_add_u64 v[214:215], s[26:27], 0, v[164:165]
	ds_read_b128 v[190:193], v187 offset:32768
	ds_read_b128 v[194:197], v187 offset:33792
	ds_read_b128 v[198:201], v187 offset:34816
	ds_read_b128 v[202:205], v187 offset:35840
	ds_read_b128 v[206:209], v187 offset:36864
	ds_read_b128 v[210:213], v187 offset:37888
	ds_read_b128 v[220:223], v187 offset:38912
	ds_read_b128 v[224:227], v187 offset:39936
	global_load_lds_dwordx4 v[214:215], off
	v_lshl_add_u64 v[214:215], s[26:27], 0, v[166:167]
	s_mov_b32 m0, s62
	s_nop 0
	global_load_lds_dwordx4 v[214:215], off
	s_waitcnt vmcnt(8)
	s_waitcnt lgkmcnt(0)
	s_barrier
	s_setprio 0
	s_waitcnt lgkmcnt(0)
	v_mfma_scale_f32_16x16x128_f8f6f4 v[158:161], v[2:9], v[190:197], v[158:161], v188, v189 op_sel_hi:[0,0,0]
	v_mfma_scale_f32_16x16x128_f8f6f4 v[154:157], v[10:17], v[190:197], v[154:157], v188, v189 op_sel_hi:[0,0,0]
	v_mfma_scale_f32_16x16x128_f8f6f4 v[150:153], v[2:9], v[198:205], v[150:153], v188, v189 op_sel_hi:[0,0,0]
	v_mfma_scale_f32_16x16x128_f8f6f4 v[146:149], v[10:17], v[198:205], v[146:149], v188, v189 op_sel_hi:[0,0,0]
	v_mfma_scale_f32_16x16x128_f8f6f4 v[138:141], v[2:9], v[206:213], v[138:141], v188, v189 op_sel_hi:[0,0,0]
	v_mfma_scale_f32_16x16x128_f8f6f4 v[130:133], v[10:17], v[206:213], v[130:133], v188, v189 op_sel_hi:[0,0,0]
	v_mfma_scale_f32_16x16x128_f8f6f4 v[122:125], v[2:9], v[220:227], v[122:125], v188, v189 op_sel_hi:[0,0,0]
	v_mfma_scale_f32_16x16x128_f8f6f4 v[114:117], v[10:17], v[220:227], v[114:117], v188, v189 op_sel_hi:[0,0,0]
	v_mfma_scale_f32_16x16x128_f8f6f4 v[142:145], v[18:25], v[190:197], v[142:145], v188, v189 op_sel_hi:[0,0,0]
	v_mfma_scale_f32_16x16x128_f8f6f4 v[134:137], v[26:33], v[190:197], v[134:137], v188, v189 op_sel_hi:[0,0,0]
	v_mfma_scale_f32_16x16x128_f8f6f4 v[126:129], v[18:25], v[198:205], v[126:129], v188, v189 op_sel_hi:[0,0,0]
	v_mfma_scale_f32_16x16x128_f8f6f4 v[118:121], v[26:33], v[198:205], v[118:121], v188, v189 op_sel_hi:[0,0,0]
	v_mfma_scale_f32_16x16x128_f8f6f4 v[110:113], v[18:25], v[206:213], v[110:113], v188, v189 op_sel_hi:[0,0,0]
	v_mfma_scale_f32_16x16x128_f8f6f4 v[106:109], v[26:33], v[206:213], v[106:109], v188, v189 op_sel_hi:[0,0,0]
	v_mfma_scale_f32_16x16x128_f8f6f4 v[102:105], v[18:25], v[220:227], v[102:105], v188, v189 op_sel_hi:[0,0,0]
	v_mfma_scale_f32_16x16x128_f8f6f4 v[98:101], v[26:33], v[220:227], v[98:101], v188, v189 op_sel_hi:[0,0,0]
	s_setprio 1
	s_barrier
	s_add_i32 s26, s54, s57
	v_lshl_add_u64 v[214:215], v[176:177], 0, s[16:17]
	s_mov_b32 m0, s26
	ds_read_b128 v[190:193], v187 offset:49152
	ds_read_b128 v[194:197], v187 offset:50176
	ds_read_b128 v[198:201], v187 offset:51200
	ds_read_b128 v[202:205], v187 offset:52224
	ds_read_b128 v[206:209], v187 offset:53248
	ds_read_b128 v[210:213], v187 offset:54272
	ds_read_b128 v[220:223], v187 offset:55296
	ds_read_b128 v[224:227], v187 offset:56320
	global_load_lds_dwordx4 v[214:215], off
	v_lshl_add_u64 v[214:215], v[176:177], 0, s[18:19]
	s_add_i32 m0, s26, 0x2000
	s_add_i32 s26, s55, s57
	global_load_lds_dwordx4 v[214:215], off
	v_lshl_add_u64 v[214:215], v[176:177], 0, s[22:23]
	s_mov_b32 m0, s26
	v_lshl_add_u64 v[176:177], v[176:177], 0, s[24:25]
	global_load_lds_dwordx4 v[214:215], off
	s_add_i32 m0, s26, 0x2000
	s_nop 0
	global_load_lds_dwordx4 v[176:177], off
	v_lshl_add_u64 v[176:177], v[178:179], 0, s[20:21]
	s_mov_b32 m0, s64
	s_nop 0
	global_load_lds_dwordx4 v[176:177], off
	v_lshl_add_u64 v[176:177], v[180:181], 0, s[20:21]
	s_mov_b32 m0, s65
	s_nop 0
	global_load_lds_dwordx4 v[176:177], off
	s_waitcnt vmcnt(8)
	s_waitcnt lgkmcnt(0)
	s_barrier
	s_setprio 0
	s_waitcnt lgkmcnt(0)
	v_mfma_scale_f32_16x16x128_f8f6f4 v[94:97], v[2:9], v[190:197], v[94:97], v188, v189 op_sel_hi:[0,0,0]
	v_mfma_scale_f32_16x16x128_f8f6f4 v[90:93], v[10:17], v[190:197], v[90:93], v188, v189 op_sel_hi:[0,0,0]
	v_mfma_scale_f32_16x16x128_f8f6f4 v[86:89], v[2:9], v[198:205], v[86:89], v188, v189 op_sel_hi:[0,0,0]
	v_mfma_scale_f32_16x16x128_f8f6f4 v[78:81], v[10:17], v[198:205], v[78:81], v188, v189 op_sel_hi:[0,0,0]
	v_mfma_scale_f32_16x16x128_f8f6f4 v[70:73], v[2:9], v[206:213], v[70:73], v188, v189 op_sel_hi:[0,0,0]
	v_mfma_scale_f32_16x16x128_f8f6f4 v[62:65], v[10:17], v[206:213], v[62:65], v188, v189 op_sel_hi:[0,0,0]
	v_mfma_scale_f32_16x16x128_f8f6f4 v[54:57], v[2:9], v[220:227], v[54:57], v188, v189 op_sel_hi:[0,0,0]
	v_mfma_scale_f32_16x16x128_f8f6f4 v[46:49], v[10:17], v[220:227], v[46:49], v188, v189 op_sel_hi:[0,0,0]
	v_mfma_scale_f32_16x16x128_f8f6f4 v[82:85], v[18:25], v[190:197], v[82:85], v188, v189 op_sel_hi:[0,0,0]
	v_mfma_scale_f32_16x16x128_f8f6f4 v[74:77], v[26:33], v[190:197], v[74:77], v188, v189 op_sel_hi:[0,0,0]
	v_mfma_scale_f32_16x16x128_f8f6f4 v[66:69], v[18:25], v[198:205], v[66:69], v188, v189 op_sel_hi:[0,0,0]
	v_mfma_scale_f32_16x16x128_f8f6f4 v[58:61], v[26:33], v[198:205], v[58:61], v188, v189 op_sel_hi:[0,0,0]
	v_mfma_scale_f32_16x16x128_f8f6f4 v[50:53], v[18:25], v[206:213], v[50:53], v188, v189 op_sel_hi:[0,0,0]
	v_mfma_scale_f32_16x16x128_f8f6f4 v[42:45], v[26:33], v[206:213], v[42:45], v188, v189 op_sel_hi:[0,0,0]
	v_mfma_scale_f32_16x16x128_f8f6f4 v[38:41], v[18:25], v[220:227], v[38:41], v188, v189 op_sel_hi:[0,0,0]
	v_mfma_scale_f32_16x16x128_f8f6f4 v[34:37], v[26:33], v[220:227], v[34:37], v188, v189 op_sel_hi:[0,0,0]
	s_setprio 1
	s_barrier
	s_add_i32 s74, s74, 2
	s_add_u32 s72, s72, 0x10000
	s_addc_u32 s73, s73, 0
	s_add_u32 s50, s50, 0x100
	s_addc_u32 s51, s51, 0
	s_cmp_gt_u32 s74, 41
	s_cbranch_scc0 .LBB0_858
	s_and_b64 vcc, exec, s[40:41]
	s_cbranch_vccz .LBB0_861
	s_barrier

.LBB0_985:
	ds_read_b128 v[26:29], v185
	ds_read_b128 v[30:33], v185 offset:1024
	ds_read_b128 v[18:21], v185 offset:2048
	ds_read_b128 v[22:25], v185 offset:3072
	ds_read_b128 v[10:13], v186
	ds_read_b128 v[14:17], v186 offset:1024
	ds_read_b128 v[2:5], v186 offset:2048
	ds_read_b128 v[6:9], v186 offset:3072
	s_add_u32 s26, s56, 0xfffc0080
	s_addc_u32 s27, s57, -1
	s_cmp_eq_u32 s80, 12
	s_cselect_b32 s59, s45, s27
	s_cselect_b32 s58, s72, s26
	s_cselect_b32 s61, s41, s75
	s_cselect_b32 s60, s73, s74
	v_lshl_add_u64 v[176:177], s[56:57], 0, v[168:169]
	s_add_i32 m0, s55, 0xc000
	ds_read_b128 v[192:195], v187
	ds_read_b128 v[196:199], v187 offset:1024
	ds_read_b128 v[200:203], v187 offset:2048
	ds_read_b128 v[204:207], v187 offset:3072
	ds_read_b128 v[208:211], v187 offset:4096
	ds_read_b128 v[212:215], v187 offset:5120
	ds_read_b128 v[220:223], v187 offset:6144
	ds_read_b128 v[224:227], v187 offset:7168
	global_load_lds_dwordx4 v[176:177], off
	v_lshl_add_u64 v[176:177], s[56:57], 0, v[170:171]
	s_add_i32 m0, s55, 0xe000
	s_nop 0
	global_load_lds_dwordx4 v[176:177], off
	s_waitcnt vmcnt(8)
	s_waitcnt lgkmcnt(0)
	s_barrier
	s_setprio 0
	s_waitcnt lgkmcnt(0)
	v_mfma_scale_f32_16x16x128_f8f6f4 v[158:161], v[26:33], v[192:199], v[158:161], v188, v189 op_sel_hi:[0,0,0]
	v_mfma_scale_f32_16x16x128_f8f6f4 v[154:157], v[18:25], v[192:199], v[154:157], v188, v189 op_sel_hi:[0,0,0]
	v_mfma_scale_f32_16x16x128_f8f6f4 v[146:149], v[26:33], v[200:207], v[146:149], v188, v189 op_sel_hi:[0,0,0]
	v_mfma_scale_f32_16x16x128_f8f6f4 v[138:141], v[18:25], v[200:207], v[138:141], v188, v189 op_sel_hi:[0,0,0]
	v_mfma_scale_f32_16x16x128_f8f6f4 v[130:133], v[26:33], v[208:215], v[130:133], v188, v189 op_sel_hi:[0,0,0]
	v_mfma_scale_f32_16x16x128_f8f6f4 v[122:125], v[18:25], v[208:215], v[122:125], v188, v189 op_sel_hi:[0,0,0]
	v_mfma_scale_f32_16x16x128_f8f6f4 v[114:117], v[26:33], v[220:227], v[114:117], v188, v189 op_sel_hi:[0,0,0]
	v_mfma_scale_f32_16x16x128_f8f6f4 v[106:109], v[18:25], v[220:227], v[106:109], v188, v189 op_sel_hi:[0,0,0]
	v_mfma_scale_f32_16x16x128_f8f6f4 v[150:153], v[10:17], v[192:199], v[150:153], v188, v189 op_sel_hi:[0,0,0]
	v_mfma_scale_f32_16x16x128_f8f6f4 v[142:145], v[2:9], v[192:199], v[142:145], v188, v189 op_sel_hi:[0,0,0]
	v_mfma_scale_f32_16x16x128_f8f6f4 v[134:137], v[10:17], v[200:207], v[134:137], v188, v189 op_sel_hi:[0,0,0]
	v_mfma_scale_f32_16x16x128_f8f6f4 v[126:129], v[2:9], v[200:207], v[126:129], v188, v189 op_sel_hi:[0,0,0]
	v_mfma_scale_f32_16x16x128_f8f6f4 v[118:121], v[10:17], v[208:215], v[118:121], v188, v189 op_sel_hi:[0,0,0]
	v_mfma_scale_f32_16x16x128_f8f6f4 v[110:113], v[2:9], v[208:215], v[110:113], v188, v189 op_sel_hi:[0,0,0]
	v_mfma_scale_f32_16x16x128_f8f6f4 v[102:105], v[10:17], v[220:227], v[102:105], v188, v189 op_sel_hi:[0,0,0]
	v_mfma_scale_f32_16x16x128_f8f6f4 v[98:101], v[2:9], v[220:227], v[98:101], v188, v189 op_sel_hi:[0,0,0]
	s_setprio 1
	s_barrier
	s_add_i32 s26, s70, s35
	v_lshl_add_u64 v[176:177], s[60:61], 0, v[162:163]
	s_mov_b32 m0, s26
	ds_read_b128 v[192:195], v187 offset:16384
	ds_read_b128 v[196:199], v187 offset:17408
	ds_read_b128 v[200:203], v187 offset:18432
	ds_read_b128 v[204:207], v187 offset:19456
	ds_read_b128 v[208:211], v187 offset:20480
	ds_read_b128 v[212:215], v187 offset:21504
	ds_read_b128 v[220:223], v187 offset:22528
	ds_read_b128 v[224:227], v187 offset:23552
	global_load_lds_dwordx4 v[176:177], off
	v_lshl_add_u64 v[178:179], v[176:177], 0, s[6:7]
	s_add_i32 m0, s26, 0x2000
	s_add_i32 s26, s71, s35
	global_load_lds_dwordx4 v[178:179], off
	v_lshl_add_u64 v[178:179], v[176:177], 0, s[8:9]
	s_mov_b32 m0, s26
	v_lshl_add_u64 v[180:181], s[58:59], 0, v[166:167]
	global_load_lds_dwordx4 v[178:179], off
	v_lshl_add_u64 v[178:179], v[176:177], 0, s[10:11]
	s_add_i32 m0, s26, 0x2000
	s_nop 0
	global_load_lds_dwordx4 v[178:179], off
	v_lshl_add_u64 v[178:179], s[58:59], 0, v[164:165]
	s_mov_b32 m0, s55
	s_nop 0
	global_load_lds_dwordx4 v[178:179], off
	s_mov_b32 m0, s63
	s_nop 0
	global_load_lds_dwordx4 v[180:181], off
	s_waitcnt vmcnt(8)
	s_waitcnt lgkmcnt(0)
	s_barrier
	s_setprio 0
	s_waitcnt lgkmcnt(0)
	v_mfma_scale_f32_16x16x128_f8f6f4 v[94:97], v[26:33], v[192:199], v[94:97], v188, v189 op_sel_hi:[0,0,0]
	v_mfma_scale_f32_16x16x128_f8f6f4 v[90:93], v[18:25], v[192:199], v[90:93], v188, v189 op_sel_hi:[0,0,0]
	v_mfma_scale_f32_16x16x128_f8f6f4 v[82:85], v[26:33], v[200:207], v[82:85], v188, v189 op_sel_hi:[0,0,0]
	v_mfma_scale_f32_16x16x128_f8f6f4 v[74:77], v[18:25], v[200:207], v[74:77], v188, v189 op_sel_hi:[0,0,0]
	v_mfma_scale_f32_16x16x128_f8f6f4 v[66:69], v[26:33], v[208:215], v[66:69], v188, v189 op_sel_hi:[0,0,0]
	v_mfma_scale_f32_16x16x128_f8f6f4 v[58:61], v[18:25], v[208:215], v[58:61], v188, v189 op_sel_hi:[0,0,0]
	v_mfma_scale_f32_16x16x128_f8f6f4 v[50:53], v[26:33], v[220:227], v[50:53], v188, v189 op_sel_hi:[0,0,0]
	v_mfma_scale_f32_16x16x128_f8f6f4 v[42:45], v[18:25], v[220:227], v[42:45], v188, v189 op_sel_hi:[0,0,0]
	v_mfma_scale_f32_16x16x128_f8f6f4 v[86:89], v[10:17], v[192:199], v[86:89], v188, v189 op_sel_hi:[0,0,0]
	v_mfma_scale_f32_16x16x128_f8f6f4 v[78:81], v[2:9], v[192:199], v[78:81], v188, v189 op_sel_hi:[0,0,0]
	v_mfma_scale_f32_16x16x128_f8f6f4 v[70:73], v[10:17], v[200:207], v[70:73], v188, v189 op_sel_hi:[0,0,0]
	v_mfma_scale_f32_16x16x128_f8f6f4 v[62:65], v[2:9], v[200:207], v[62:65], v188, v189 op_sel_hi:[0,0,0]
	v_mfma_scale_f32_16x16x128_f8f6f4 v[54:57], v[10:17], v[208:215], v[54:57], v188, v189 op_sel_hi:[0,0,0]
	v_mfma_scale_f32_16x16x128_f8f6f4 v[46:49], v[2:9], v[208:215], v[46:49], v188, v189 op_sel_hi:[0,0,0]
	v_mfma_scale_f32_16x16x128_f8f6f4 v[38:41], v[10:17], v[220:227], v[38:41], v188, v189 op_sel_hi:[0,0,0]
	v_mfma_scale_f32_16x16x128_f8f6f4 v[34:37], v[2:9], v[220:227], v[34:37], v188, v189 op_sel_hi:[0,0,0]
	s_setprio 1
	s_barrier
	s_add_i32 s60, 0, 0x18000
	s_add_i32 s61, 0, 0x1c000
	v_add_u32_e32 v14, s60, v183
	v_add_u32_e32 v30, s61, v183
	ds_read_b128 v[2:5], v14
	ds_read_b128 v[6:9], v14 offset:1024
	ds_read_b128 v[10:13], v14 offset:2048
	ds_read_b128 v[14:17], v14 offset:3072
	ds_read_b128 v[18:21], v30
	ds_read_b128 v[22:25], v30 offset:1024
	ds_read_b128 v[26:29], v30 offset:2048
	ds_read_b128 v[30:33], v30 offset:3072
	s_add_u32 s26, s58, 0x40000
	s_addc_u32 s27, s59, 0
	s_mov_b32 m0, s64
	v_lshl_add_u64 v[216:217], s[26:27], 0, v[164:165]
	ds_read_b128 v[192:195], v187 offset:32768
	ds_read_b128 v[196:199], v187 offset:33792
	ds_read_b128 v[200:203], v187 offset:34816
	ds_read_b128 v[204:207], v187 offset:35840
	ds_read_b128 v[208:211], v187 offset:36864
	ds_read_b128 v[212:215], v187 offset:37888
	ds_read_b128 v[220:223], v187 offset:38912
	ds_read_b128 v[224:227], v187 offset:39936
	global_load_lds_dwordx4 v[216:217], off
	v_lshl_add_u64 v[216:217], s[26:27], 0, v[166:167]
	s_mov_b32 m0, s65
	s_nop 0
	global_load_lds_dwordx4 v[216:217], off
	s_waitcnt vmcnt(8)
	s_waitcnt lgkmcnt(0)
	s_barrier
	s_setprio 0
	s_waitcnt lgkmcnt(0)
	v_mfma_scale_f32_16x16x128_f8f6f4 v[158:161], v[2:9], v[192:199], v[158:161], v188, v189 op_sel_hi:[0,0,0]
	v_mfma_scale_f32_16x16x128_f8f6f4 v[154:157], v[10:17], v[192:199], v[154:157], v188, v189 op_sel_hi:[0,0,0]
	v_mfma_scale_f32_16x16x128_f8f6f4 v[146:149], v[2:9], v[200:207], v[146:149], v188, v189 op_sel_hi:[0,0,0]
	v_mfma_scale_f32_16x16x128_f8f6f4 v[138:141], v[10:17], v[200:207], v[138:141], v188, v189 op_sel_hi:[0,0,0]
	v_mfma_scale_f32_16x16x128_f8f6f4 v[130:133], v[2:9], v[208:215], v[130:133], v188, v189 op_sel_hi:[0,0,0]
	v_mfma_scale_f32_16x16x128_f8f6f4 v[122:125], v[10:17], v[208:215], v[122:125], v188, v189 op_sel_hi:[0,0,0]
	v_mfma_scale_f32_16x16x128_f8f6f4 v[114:117], v[2:9], v[220:227], v[114:117], v188, v189 op_sel_hi:[0,0,0]
	v_mfma_scale_f32_16x16x128_f8f6f4 v[106:109], v[10:17], v[220:227], v[106:109], v188, v189 op_sel_hi:[0,0,0]
	v_mfma_scale_f32_16x16x128_f8f6f4 v[150:153], v[18:25], v[192:199], v[150:153], v188, v189 op_sel_hi:[0,0,0]
	v_mfma_scale_f32_16x16x128_f8f6f4 v[142:145], v[26:33], v[192:199], v[142:145], v188, v189 op_sel_hi:[0,0,0]
	v_mfma_scale_f32_16x16x128_f8f6f4 v[134:137], v[18:25], v[200:207], v[134:137], v188, v189 op_sel_hi:[0,0,0]
	v_mfma_scale_f32_16x16x128_f8f6f4 v[126:129], v[26:33], v[200:207], v[126:129], v188, v189 op_sel_hi:[0,0,0]
	v_mfma_scale_f32_16x16x128_f8f6f4 v[118:121], v[18:25], v[208:215], v[118:121], v188, v189 op_sel_hi:[0,0,0]
	v_mfma_scale_f32_16x16x128_f8f6f4 v[110:113], v[26:33], v[208:215], v[110:113], v188, v189 op_sel_hi:[0,0,0]
	v_mfma_scale_f32_16x16x128_f8f6f4 v[102:105], v[18:25], v[220:227], v[102:105], v188, v189 op_sel_hi:[0,0,0]
	v_mfma_scale_f32_16x16x128_f8f6f4 v[98:101], v[26:33], v[220:227], v[98:101], v188, v189 op_sel_hi:[0,0,0]
	s_setprio 1
	s_barrier
	s_add_i32 s26, s60, s35
	v_lshl_add_u64 v[216:217], v[176:177], 0, s[14:15]
	s_mov_b32 m0, s26
	ds_read_b128 v[192:195], v187 offset:49152
	ds_read_b128 v[196:199], v187 offset:50176
	ds_read_b128 v[200:203], v187 offset:51200
	ds_read_b128 v[204:207], v187 offset:52224
	ds_read_b128 v[208:211], v187 offset:53248
	ds_read_b128 v[212:215], v187 offset:54272
	ds_read_b128 v[220:223], v187 offset:55296
	ds_read_b128 v[224:227], v187 offset:56320
	global_load_lds_dwordx4 v[216:217], off
	v_lshl_add_u64 v[216:217], v[176:177], 0, s[16:17]
	s_add_i32 m0, s26, 0x2000
	s_add_i32 s26, s61, s35
	global_load_lds_dwordx4 v[216:217], off
	v_lshl_add_u64 v[216:217], v[176:177], 0, s[20:21]
	s_mov_b32 m0, s26
	v_lshl_add_u64 v[176:177], v[176:177], 0, s[22:23]
	global_load_lds_dwordx4 v[216:217], off
	s_add_i32 m0, s26, 0x2000
	s_nop 0
	global_load_lds_dwordx4 v[176:177], off
	v_lshl_add_u64 v[176:177], v[178:179], 0, s[18:19]
	s_mov_b32 m0, s67
	s_nop 0
	global_load_lds_dwordx4 v[176:177], off
	v_lshl_add_u64 v[176:177], v[180:181], 0, s[18:19]
	s_mov_b32 m0, s68
	s_nop 0
	global_load_lds_dwordx4 v[176:177], off
	s_waitcnt vmcnt(8)
	s_waitcnt lgkmcnt(0)
	s_barrier
	s_setprio 0
	s_waitcnt lgkmcnt(0)
	v_mfma_scale_f32_16x16x128_f8f6f4 v[94:97], v[2:9], v[192:199], v[94:97], v188, v189 op_sel_hi:[0,0,0]
	v_mfma_scale_f32_16x16x128_f8f6f4 v[90:93], v[10:17], v[192:199], v[90:93], v188, v189 op_sel_hi:[0,0,0]
	v_mfma_scale_f32_16x16x128_f8f6f4 v[82:85], v[2:9], v[200:207], v[82:85], v188, v189 op_sel_hi:[0,0,0]
	v_mfma_scale_f32_16x16x128_f8f6f4 v[74:77], v[10:17], v[200:207], v[74:77], v188, v189 op_sel_hi:[0,0,0]
	v_mfma_scale_f32_16x16x128_f8f6f4 v[66:69], v[2:9], v[208:215], v[66:69], v188, v189 op_sel_hi:[0,0,0]
	v_mfma_scale_f32_16x16x128_f8f6f4 v[58:61], v[10:17], v[208:215], v[58:61], v188, v189 op_sel_hi:[0,0,0]
	v_mfma_scale_f32_16x16x128_f8f6f4 v[50:53], v[2:9], v[220:227], v[50:53], v188, v189 op_sel_hi:[0,0,0]
	v_mfma_scale_f32_16x16x128_f8f6f4 v[42:45], v[10:17], v[220:227], v[42:45], v188, v189 op_sel_hi:[0,0,0]
	v_mfma_scale_f32_16x16x128_f8f6f4 v[86:89], v[18:25], v[192:199], v[86:89], v188, v189 op_sel_hi:[0,0,0]
	v_mfma_scale_f32_16x16x128_f8f6f4 v[78:81], v[26:33], v[192:199], v[78:81], v188, v189 op_sel_hi:[0,0,0]
	v_mfma_scale_f32_16x16x128_f8f6f4 v[70:73], v[18:25], v[200:207], v[70:73], v188, v189 op_sel_hi:[0,0,0]
	v_mfma_scale_f32_16x16x128_f8f6f4 v[62:65], v[26:33], v[200:207], v[62:65], v188, v189 op_sel_hi:[0,0,0]
	v_mfma_scale_f32_16x16x128_f8f6f4 v[54:57], v[18:25], v[208:215], v[54:57], v188, v189 op_sel_hi:[0,0,0]
	v_mfma_scale_f32_16x16x128_f8f6f4 v[46:49], v[26:33], v[208:215], v[46:49], v188, v189 op_sel_hi:[0,0,0]
	v_mfma_scale_f32_16x16x128_f8f6f4 v[38:41], v[18:25], v[220:227], v[38:41], v188, v189 op_sel_hi:[0,0,0]
	v_mfma_scale_f32_16x16x128_f8f6f4 v[34:37], v[26:33], v[220:227], v[34:37], v188, v189 op_sel_hi:[0,0,0]
	s_setprio 1
	s_barrier
	s_add_i32 s80, s80, 2
	s_add_u32 s74, s74, 0x10000
	s_addc_u32 s75, s75, 0
	s_add_u32 s56, s56, 0x100
	s_addc_u32 s57, s57, 0
	s_cmp_gt_u32 s80, 13
	s_cbranch_scc0 .LBB0_985
	s_and_b64 vcc, exec, s[24:25]
	s_cbranch_vccz .LBB0_988
	s_barrier

.LBB0_1192:
	ds_read_b128 v[66:69], v199
	ds_read_b128 v[70:73], v199 offset:1024
	ds_read_b128 v[82:85], v199 offset:2048
	ds_read_b128 v[86:89], v199 offset:3072
	ds_read_b128 v[146:149], v200
	ds_read_b128 v[150:153], v200 offset:1024
	ds_read_b128 v[154:157], v200 offset:2048
	ds_read_b128 v[158:161], v200 offset:3072
	s_add_u32 s26, s56, 0xfffc0080
	s_addc_u32 s27, s57, -1
	s_cmp_eq_u32 s73, 12
	s_cselect_b32 s59, s45, s27
	s_cselect_b32 s58, s69, s26
	s_cselect_b32 s27, s41, s72
	s_cselect_b32 s26, s70, s71
	v_lshl_add_u64 v[214:215], s[56:57], 0, v[176:177]
	s_add_i32 m0, s55, 0xc000
	ds_read_b128 v[162:165], v201
	ds_read_b128 v[166:169], v201 offset:1024
	ds_read_b128 v[184:187], v201 offset:2048
	ds_read_b128 v[188:191], v201 offset:3072
	ds_read_b128 v[192:195], v201 offset:4096
	ds_read_b128 v[202:205], v201 offset:5120
	ds_read_b128 v[206:209], v201 offset:6144
	ds_read_b128 v[210:213], v201 offset:7168
	global_load_lds_dwordx4 v[214:215], off
	v_lshl_add_u64 v[214:215], s[56:57], 0, v[178:179]
	s_add_i32 m0, s55, 0xe000
	s_nop 0
	global_load_lds_dwordx4 v[214:215], off
	s_waitcnt vmcnt(8)
	s_waitcnt lgkmcnt(0)
	s_barrier
	s_setprio 0
	s_waitcnt lgkmcnt(0)
	v_mfma_f32_16x16x32_bf16 v[142:145], v[66:69], v[162:165], v[142:145]
	v_mfma_f32_16x16x32_bf16 v[138:141], v[82:85], v[162:165], v[138:141]
	v_mfma_f32_16x16x32_bf16 v[126:129], v[66:69], v[184:187], v[126:129]
	v_mfma_f32_16x16x32_bf16 v[122:125], v[82:85], v[184:187], v[122:125]
	v_mfma_f32_16x16x32_bf16 v[110:113], v[66:69], v[192:195], v[110:113]
	v_mfma_f32_16x16x32_bf16 v[106:109], v[82:85], v[192:195], v[106:109]
	v_mfma_f32_16x16x32_bf16 v[94:97], v[66:69], v[206:209], v[94:97]
	v_mfma_f32_16x16x32_bf16 v[90:93], v[82:85], v[206:209], v[90:93]
	v_mfma_f32_16x16x32_bf16 v[142:145], v[70:73], v[166:169], v[142:145]
	v_mfma_f32_16x16x32_bf16 v[138:141], v[86:89], v[166:169], v[138:141]
	v_mfma_f32_16x16x32_bf16 v[126:129], v[70:73], v[188:191], v[126:129]
	v_mfma_f32_16x16x32_bf16 v[122:125], v[86:89], v[188:191], v[122:125]
	v_mfma_f32_16x16x32_bf16 v[110:113], v[70:73], v[202:205], v[110:113]
	v_mfma_f32_16x16x32_bf16 v[106:109], v[86:89], v[202:205], v[106:109]
	v_mfma_f32_16x16x32_bf16 v[94:97], v[70:73], v[210:213], v[94:97]
	v_mfma_f32_16x16x32_bf16 v[90:93], v[86:89], v[210:213], v[90:93]
	v_mfma_f32_16x16x32_bf16 v[134:137], v[146:149], v[162:165], v[134:137]
	v_mfma_f32_16x16x32_bf16 v[130:133], v[154:157], v[162:165], v[130:133]
	v_mfma_f32_16x16x32_bf16 v[118:121], v[146:149], v[184:187], v[118:121]
	v_mfma_f32_16x16x32_bf16 v[114:117], v[154:157], v[184:187], v[114:117]
	v_mfma_f32_16x16x32_bf16 v[102:105], v[146:149], v[192:195], v[102:105]
	v_mfma_f32_16x16x32_bf16 v[98:101], v[154:157], v[192:195], v[98:101]
	v_mfma_f32_16x16x32_bf16 v[78:81], v[146:149], v[206:209], v[78:81]
	v_mfma_f32_16x16x32_bf16 v[74:77], v[154:157], v[206:209], v[74:77]
	v_mfma_f32_16x16x32_bf16 v[134:137], v[150:153], v[166:169], v[134:137]
	v_mfma_f32_16x16x32_bf16 v[130:133], v[158:161], v[166:169], v[130:133]
	v_mfma_f32_16x16x32_bf16 v[118:121], v[150:153], v[188:191], v[118:121]
	v_mfma_f32_16x16x32_bf16 v[114:117], v[158:161], v[188:191], v[114:117]
	v_mfma_f32_16x16x32_bf16 v[102:105], v[150:153], v[202:205], v[102:105]
	v_mfma_f32_16x16x32_bf16 v[98:101], v[158:161], v[202:205], v[98:101]
	v_mfma_f32_16x16x32_bf16 v[78:81], v[150:153], v[210:213], v[78:81]
	v_mfma_f32_16x16x32_bf16 v[74:77], v[158:161], v[210:213], v[74:77]
	s_setprio 1
	s_barrier
	v_lshl_add_u64 v[214:215], s[26:27], 0, v[170:171]
	s_add_i32 s26, s67, s35
	s_mov_b32 m0, s26
	ds_read_b128 v[162:165], v201 offset:16384
	ds_read_b128 v[166:169], v201 offset:17408
	ds_read_b128 v[184:187], v201 offset:18432
	ds_read_b128 v[188:191], v201 offset:19456
	ds_read_b128 v[192:195], v201 offset:20480
	ds_read_b128 v[202:205], v201 offset:21504
	ds_read_b128 v[206:209], v201 offset:22528
	ds_read_b128 v[210:213], v201 offset:23552
	global_load_lds_dwordx4 v[214:215], off
	v_lshl_add_u64 v[216:217], v[214:215], 0, s[6:7]
	s_add_i32 m0, s26, 0x2000
	s_add_i32 s26, s68, s35
	global_load_lds_dwordx4 v[216:217], off
	v_lshl_add_u64 v[216:217], v[214:215], 0, s[10:11]
	s_mov_b32 m0, s26
	v_lshl_add_u64 v[220:221], s[58:59], 0, v[174:175]
	global_load_lds_dwordx4 v[216:217], off
	v_lshl_add_u64 v[216:217], v[214:215], 0, s[12:13]
	s_add_i32 m0, s26, 0x2000
	s_nop 0
	global_load_lds_dwordx4 v[216:217], off
	v_lshl_add_u64 v[216:217], s[58:59], 0, v[172:173]
	s_mov_b32 m0, s55
	s_nop 0
	global_load_lds_dwordx4 v[216:217], off
	s_mov_b32 m0, s60
	s_nop 0
	global_load_lds_dwordx4 v[220:221], off
	s_waitcnt vmcnt(8)
	s_waitcnt lgkmcnt(0)
	s_barrier
	s_setprio 0
	s_waitcnt lgkmcnt(0)
	v_mfma_f32_16x16x32_bf16 v[62:65], v[66:69], v[162:165], v[62:65]
	v_mfma_f32_16x16x32_bf16 v[58:61], v[82:85], v[162:165], v[58:61]
	v_mfma_f32_16x16x32_bf16 v[46:49], v[66:69], v[184:187], v[46:49]
	v_mfma_f32_16x16x32_bf16 v[42:45], v[82:85], v[184:187], v[42:45]
	v_mfma_f32_16x16x32_bf16 v[30:33], v[66:69], v[192:195], v[30:33]
	v_mfma_f32_16x16x32_bf16 v[26:29], v[82:85], v[192:195], v[26:29]
	v_mfma_f32_16x16x32_bf16 v[14:17], v[66:69], v[206:209], v[14:17]
	v_mfma_f32_16x16x32_bf16 v[10:13], v[82:85], v[206:209], v[10:13]
	v_mfma_f32_16x16x32_bf16 v[62:65], v[70:73], v[166:169], v[62:65]
	v_mfma_f32_16x16x32_bf16 v[58:61], v[86:89], v[166:169], v[58:61]
	v_mfma_f32_16x16x32_bf16 v[46:49], v[70:73], v[188:191], v[46:49]
	v_mfma_f32_16x16x32_bf16 v[42:45], v[86:89], v[188:191], v[42:45]
	v_mfma_f32_16x16x32_bf16 v[30:33], v[70:73], v[202:205], v[30:33]
	v_mfma_f32_16x16x32_bf16 v[26:29], v[86:89], v[202:205], v[26:29]
	v_mfma_f32_16x16x32_bf16 v[14:17], v[70:73], v[210:213], v[14:17]
	v_mfma_f32_16x16x32_bf16 v[10:13], v[86:89], v[210:213], v[10:13]
	v_mfma_f32_16x16x32_bf16 v[54:57], v[146:149], v[162:165], v[54:57]
	v_mfma_f32_16x16x32_bf16 v[50:53], v[154:157], v[162:165], v[50:53]
	v_mfma_f32_16x16x32_bf16 v[38:41], v[146:149], v[184:187], v[38:41]
	v_mfma_f32_16x16x32_bf16 v[34:37], v[154:157], v[184:187], v[34:37]
	v_mfma_f32_16x16x32_bf16 v[22:25], v[146:149], v[192:195], v[22:25]
	v_mfma_f32_16x16x32_bf16 v[18:21], v[154:157], v[192:195], v[18:21]
	v_mfma_f32_16x16x32_bf16 v[6:9], v[146:149], v[206:209], v[6:9]
	v_mfma_f32_16x16x32_bf16 v[2:5], v[154:157], v[206:209], v[2:5]
	v_mfma_f32_16x16x32_bf16 v[54:57], v[150:153], v[166:169], v[54:57]
	v_mfma_f32_16x16x32_bf16 v[50:53], v[158:161], v[166:169], v[50:53]
	v_mfma_f32_16x16x32_bf16 v[38:41], v[150:153], v[188:191], v[38:41]
	v_mfma_f32_16x16x32_bf16 v[34:37], v[158:161], v[188:191], v[34:37]
	v_mfma_f32_16x16x32_bf16 v[22:25], v[150:153], v[202:205], v[22:25]
	v_mfma_f32_16x16x32_bf16 v[18:21], v[158:161], v[202:205], v[18:21]
	v_mfma_f32_16x16x32_bf16 v[6:9], v[150:153], v[210:213], v[6:9]
	v_mfma_f32_16x16x32_bf16 v[2:5], v[158:161], v[210:213], v[2:5]
	s_setprio 1
	s_barrier
	s_add_i32 s74, 0, 0x18000
	s_add_i32 s75, 0, 0x1c000
	v_add_u32_e32 v86, s74, v197
	v_add_u32_e32 v158, s75, v197
	ds_read_b128 v[66:69], v86
	ds_read_b128 v[70:73], v86 offset:1024
	ds_read_b128 v[82:85], v86 offset:2048
	ds_read_b128 v[86:89], v86 offset:3072
	ds_read_b128 v[146:149], v158
	ds_read_b128 v[150:153], v158 offset:1024
	ds_read_b128 v[154:157], v158 offset:2048
	ds_read_b128 v[158:161], v158 offset:3072
	s_add_u32 s26, s58, 0x40000
	s_addc_u32 s27, s59, 0
	s_mov_b32 m0, s61
	v_lshl_add_u64 v[222:223], s[26:27], 0, v[172:173]
	ds_read_b128 v[162:165], v201 offset:32768
	ds_read_b128 v[166:169], v201 offset:33792
	ds_read_b128 v[184:187], v201 offset:34816
	ds_read_b128 v[188:191], v201 offset:35840
	ds_read_b128 v[192:195], v201 offset:36864
	ds_read_b128 v[202:205], v201 offset:37888
	ds_read_b128 v[206:209], v201 offset:38912
	ds_read_b128 v[210:213], v201 offset:39936
	global_load_lds_dwordx4 v[222:223], off
	v_lshl_add_u64 v[222:223], s[26:27], 0, v[174:175]
	s_mov_b32 m0, s62
	s_nop 0
	global_load_lds_dwordx4 v[222:223], off
	s_waitcnt vmcnt(8)
	s_waitcnt lgkmcnt(0)
	s_barrier
	s_setprio 0
	s_waitcnt lgkmcnt(0)
	v_mfma_f32_16x16x32_bf16 v[142:145], v[66:69], v[162:165], v[142:145]
	v_mfma_f32_16x16x32_bf16 v[138:141], v[82:85], v[162:165], v[138:141]
	v_mfma_f32_16x16x32_bf16 v[126:129], v[66:69], v[184:187], v[126:129]
	v_mfma_f32_16x16x32_bf16 v[122:125], v[82:85], v[184:187], v[122:125]
	v_mfma_f32_16x16x32_bf16 v[110:113], v[66:69], v[192:195], v[110:113]
	v_mfma_f32_16x16x32_bf16 v[106:109], v[82:85], v[192:195], v[106:109]
	v_mfma_f32_16x16x32_bf16 v[94:97], v[66:69], v[206:209], v[94:97]
	v_mfma_f32_16x16x32_bf16 v[90:93], v[82:85], v[206:209], v[90:93]
	v_mfma_f32_16x16x32_bf16 v[142:145], v[70:73], v[166:169], v[142:145]
	v_mfma_f32_16x16x32_bf16 v[138:141], v[86:89], v[166:169], v[138:141]
	v_mfma_f32_16x16x32_bf16 v[126:129], v[70:73], v[188:191], v[126:129]
	v_mfma_f32_16x16x32_bf16 v[122:125], v[86:89], v[188:191], v[122:125]
	v_mfma_f32_16x16x32_bf16 v[110:113], v[70:73], v[202:205], v[110:113]
	v_mfma_f32_16x16x32_bf16 v[106:109], v[86:89], v[202:205], v[106:109]
	v_mfma_f32_16x16x32_bf16 v[94:97], v[70:73], v[210:213], v[94:97]
	v_mfma_f32_16x16x32_bf16 v[90:93], v[86:89], v[210:213], v[90:93]
	v_mfma_f32_16x16x32_bf16 v[134:137], v[146:149], v[162:165], v[134:137]
	v_mfma_f32_16x16x32_bf16 v[130:133], v[154:157], v[162:165], v[130:133]
	v_mfma_f32_16x16x32_bf16 v[118:121], v[146:149], v[184:187], v[118:121]
	v_mfma_f32_16x16x32_bf16 v[114:117], v[154:157], v[184:187], v[114:117]
	v_mfma_f32_16x16x32_bf16 v[102:105], v[146:149], v[192:195], v[102:105]
	v_mfma_f32_16x16x32_bf16 v[98:101], v[154:157], v[192:195], v[98:101]
	v_mfma_f32_16x16x32_bf16 v[78:81], v[146:149], v[206:209], v[78:81]
	v_mfma_f32_16x16x32_bf16 v[74:77], v[154:157], v[206:209], v[74:77]
	v_mfma_f32_16x16x32_bf16 v[134:137], v[150:153], v[166:169], v[134:137]
	v_mfma_f32_16x16x32_bf16 v[130:133], v[158:161], v[166:169], v[130:133]
	v_mfma_f32_16x16x32_bf16 v[118:121], v[150:153], v[188:191], v[118:121]
	v_mfma_f32_16x16x32_bf16 v[114:117], v[158:161], v[188:191], v[114:117]
	v_mfma_f32_16x16x32_bf16 v[102:105], v[150:153], v[202:205], v[102:105]
	v_mfma_f32_16x16x32_bf16 v[98:101], v[158:161], v[202:205], v[98:101]
	v_mfma_f32_16x16x32_bf16 v[78:81], v[150:153], v[210:213], v[78:81]
	v_mfma_f32_16x16x32_bf16 v[74:77], v[158:161], v[210:213], v[74:77]
	s_setprio 1
	s_barrier
	s_add_i32 s26, s74, s35
	v_lshl_add_u64 v[222:223], v[214:215], 0, s[16:17]
	s_mov_b32 m0, s26
	ds_read_b128 v[162:165], v201 offset:49152
	ds_read_b128 v[166:169], v201 offset:50176
	ds_read_b128 v[184:187], v201 offset:51200
	ds_read_b128 v[188:191], v201 offset:52224
	ds_read_b128 v[192:195], v201 offset:53248
	ds_read_b128 v[202:205], v201 offset:54272
	ds_read_b128 v[206:209], v201 offset:55296
	ds_read_b128 v[210:213], v201 offset:56320
	global_load_lds_dwordx4 v[222:223], off
	v_lshl_add_u64 v[222:223], v[214:215], 0, s[18:19]
	s_add_i32 m0, s26, 0x2000
	s_add_i32 s26, s75, s35
	global_load_lds_dwordx4 v[222:223], off
	v_lshl_add_u64 v[222:223], v[214:215], 0, s[22:23]
	s_mov_b32 m0, s26
	v_lshl_add_u64 v[214:215], v[214:215], 0, s[24:25]
	global_load_lds_dwordx4 v[222:223], off
	s_add_i32 m0, s26, 0x2000
	s_nop 0
	global_load_lds_dwordx4 v[214:215], off
	v_lshl_add_u64 v[214:215], v[216:217], 0, s[20:21]
	s_mov_b32 m0, s64
	s_nop 0
	global_load_lds_dwordx4 v[214:215], off
	v_lshl_add_u64 v[214:215], v[220:221], 0, s[20:21]
	s_mov_b32 m0, s65
	s_nop 0
	global_load_lds_dwordx4 v[214:215], off
	s_waitcnt vmcnt(8)
	s_waitcnt lgkmcnt(0)
	s_barrier
	s_setprio 0
	s_waitcnt lgkmcnt(0)
	v_mfma_f32_16x16x32_bf16 v[62:65], v[66:69], v[162:165], v[62:65]
	v_mfma_f32_16x16x32_bf16 v[58:61], v[82:85], v[162:165], v[58:61]
	v_mfma_f32_16x16x32_bf16 v[46:49], v[66:69], v[184:187], v[46:49]
	v_mfma_f32_16x16x32_bf16 v[42:45], v[82:85], v[184:187], v[42:45]
	v_mfma_f32_16x16x32_bf16 v[30:33], v[66:69], v[192:195], v[30:33]
	v_mfma_f32_16x16x32_bf16 v[26:29], v[82:85], v[192:195], v[26:29]
	v_mfma_f32_16x16x32_bf16 v[14:17], v[66:69], v[206:209], v[14:17]
	v_mfma_f32_16x16x32_bf16 v[10:13], v[82:85], v[206:209], v[10:13]
	v_mfma_f32_16x16x32_bf16 v[62:65], v[70:73], v[166:169], v[62:65]
	v_mfma_f32_16x16x32_bf16 v[58:61], v[86:89], v[166:169], v[58:61]
	v_mfma_f32_16x16x32_bf16 v[46:49], v[70:73], v[188:191], v[46:49]
	v_mfma_f32_16x16x32_bf16 v[42:45], v[86:89], v[188:191], v[42:45]
	v_mfma_f32_16x16x32_bf16 v[30:33], v[70:73], v[202:205], v[30:33]
	v_mfma_f32_16x16x32_bf16 v[26:29], v[86:89], v[202:205], v[26:29]
	v_mfma_f32_16x16x32_bf16 v[14:17], v[70:73], v[210:213], v[14:17]
	v_mfma_f32_16x16x32_bf16 v[10:13], v[86:89], v[210:213], v[10:13]
	v_mfma_f32_16x16x32_bf16 v[54:57], v[146:149], v[162:165], v[54:57]
	v_mfma_f32_16x16x32_bf16 v[50:53], v[154:157], v[162:165], v[50:53]
	v_mfma_f32_16x16x32_bf16 v[38:41], v[146:149], v[184:187], v[38:41]
	v_mfma_f32_16x16x32_bf16 v[34:37], v[154:157], v[184:187], v[34:37]
	v_mfma_f32_16x16x32_bf16 v[22:25], v[146:149], v[192:195], v[22:25]
	v_mfma_f32_16x16x32_bf16 v[18:21], v[154:157], v[192:195], v[18:21]
	v_mfma_f32_16x16x32_bf16 v[6:9], v[146:149], v[206:209], v[6:9]
	v_mfma_f32_16x16x32_bf16 v[2:5], v[154:157], v[206:209], v[2:5]
	v_mfma_f32_16x16x32_bf16 v[54:57], v[150:153], v[166:169], v[54:57]
	v_mfma_f32_16x16x32_bf16 v[50:53], v[158:161], v[166:169], v[50:53]
	v_mfma_f32_16x16x32_bf16 v[38:41], v[150:153], v[188:191], v[38:41]
	v_mfma_f32_16x16x32_bf16 v[34:37], v[158:161], v[188:191], v[34:37]
	v_mfma_f32_16x16x32_bf16 v[22:25], v[150:153], v[202:205], v[22:25]
	v_mfma_f32_16x16x32_bf16 v[18:21], v[158:161], v[202:205], v[18:21]
	v_mfma_f32_16x16x32_bf16 v[6:9], v[150:153], v[210:213], v[6:9]
	v_mfma_f32_16x16x32_bf16 v[2:5], v[158:161], v[210:213], v[2:5]
	s_setprio 1
	s_barrier
	s_add_i32 s73, s73, 2
	s_add_u32 s71, s71, 0x10000
	s_addc_u32 s72, s72, 0
	s_add_u32 s56, s56, 0x100
	s_addc_u32 s57, s57, 0
	s_cmp_gt_u32 s73, 13
	s_cbranch_scc0 .LBB0_1192
	s_and_b64 vcc, exec, s[36:37]
	s_cbranch_vccz .LBB0_1195
	s_barrier

.LBB0_1271:
	ds_read_b128 v[144:147], v158
	ds_read_b128 v[148:151], v158 offset:1024
	ds_read_b128 v[152:155], v158 offset:2048
	ds_read_b128 v[162:165], v158 offset:3072
	ds_read_b128 v[166:169], v159
	ds_read_b128 v[170:173], v159 offset:1024
	ds_read_b128 v[174:177], v159 offset:2048
	ds_read_b128 v[178:181], v159 offset:3072
	s_add_u32 s26, s58, 0xfff80080
	s_addc_u32 s27, s59, -1
	s_cmp_eq_u32 s80, 28
	s_cselect_b32 s61, s51, s27
	s_cselect_b32 s60, s57, s26
	s_cselect_b32 s27, s45, s75
	s_cselect_b32 s26, s73, s74
	v_lshl_add_u64 v[214:215], s[58:59], 0, v[136:137]
	s_add_i32 m0, s63, 0xc000
	ds_read_b128 v[182:185], v160
	ds_read_b128 v[186:189], v160 offset:1024
	ds_read_b128 v[190:193], v160 offset:2048
	ds_read_b128 v[194:197], v160 offset:3072
	ds_read_b128 v[198:201], v160 offset:4096
	ds_read_b128 v[202:205], v160 offset:5120
	ds_read_b128 v[206:209], v160 offset:6144
	ds_read_b128 v[210:213], v160 offset:7168
	global_load_lds_dwordx4 v[214:215], off
	v_lshl_add_u64 v[214:215], s[58:59], 0, v[138:139]
	s_add_i32 m0, s63, 0xe000
	s_nop 0
	global_load_lds_dwordx4 v[214:215], off
	s_waitcnt vmcnt(8)
	s_waitcnt lgkmcnt(0)
	s_barrier
	s_setprio 0
	s_waitcnt lgkmcnt(0)
	v_mfma_f32_16x16x32_bf16 v[126:129], v[144:147], v[182:185], v[126:129]
	v_mfma_f32_16x16x32_bf16 v[122:125], v[152:155], v[182:185], v[122:125]
	v_mfma_f32_16x16x32_bf16 v[118:121], v[144:147], v[190:193], v[118:121]
	v_mfma_f32_16x16x32_bf16 v[114:117], v[152:155], v[190:193], v[114:117]
	v_mfma_f32_16x16x32_bf16 v[106:109], v[144:147], v[198:201], v[106:109]
	v_mfma_f32_16x16x32_bf16 v[98:101], v[152:155], v[198:201], v[98:101]
	v_mfma_f32_16x16x32_bf16 v[90:93], v[144:147], v[206:209], v[90:93]
	v_mfma_f32_16x16x32_bf16 v[82:85], v[152:155], v[206:209], v[82:85]
	v_mfma_f32_16x16x32_bf16 v[126:129], v[148:151], v[186:189], v[126:129]
	v_mfma_f32_16x16x32_bf16 v[122:125], v[162:165], v[186:189], v[122:125]
	v_mfma_f32_16x16x32_bf16 v[118:121], v[148:151], v[194:197], v[118:121]
	v_mfma_f32_16x16x32_bf16 v[114:117], v[162:165], v[194:197], v[114:117]
	v_mfma_f32_16x16x32_bf16 v[106:109], v[148:151], v[202:205], v[106:109]
	v_mfma_f32_16x16x32_bf16 v[98:101], v[162:165], v[202:205], v[98:101]
	v_mfma_f32_16x16x32_bf16 v[90:93], v[148:151], v[210:213], v[90:93]
	v_mfma_f32_16x16x32_bf16 v[82:85], v[162:165], v[210:213], v[82:85]
	v_mfma_f32_16x16x32_bf16 v[110:113], v[166:169], v[182:185], v[110:113]
	v_mfma_f32_16x16x32_bf16 v[102:105], v[174:177], v[182:185], v[102:105]
	v_mfma_f32_16x16x32_bf16 v[94:97], v[166:169], v[190:193], v[94:97]
	v_mfma_f32_16x16x32_bf16 v[86:89], v[174:177], v[190:193], v[86:89]
	v_mfma_f32_16x16x32_bf16 v[78:81], v[166:169], v[198:201], v[78:81]
	v_mfma_f32_16x16x32_bf16 v[74:77], v[174:177], v[198:201], v[74:77]
	v_mfma_f32_16x16x32_bf16 v[70:73], v[166:169], v[206:209], v[70:73]
	v_mfma_f32_16x16x32_bf16 v[66:69], v[174:177], v[206:209], v[66:69]
	v_mfma_f32_16x16x32_bf16 v[110:113], v[170:173], v[186:189], v[110:113]
	v_mfma_f32_16x16x32_bf16 v[102:105], v[178:181], v[186:189], v[102:105]
	v_mfma_f32_16x16x32_bf16 v[94:97], v[170:173], v[194:197], v[94:97]
	v_mfma_f32_16x16x32_bf16 v[86:89], v[178:181], v[194:197], v[86:89]
	v_mfma_f32_16x16x32_bf16 v[78:81], v[170:173], v[202:205], v[78:81]
	v_mfma_f32_16x16x32_bf16 v[74:77], v[178:181], v[202:205], v[74:77]
	v_mfma_f32_16x16x32_bf16 v[70:73], v[170:173], v[210:213], v[70:73]
	v_mfma_f32_16x16x32_bf16 v[66:69], v[178:181], v[210:213], v[66:69]
	s_setprio 1
	s_barrier
	v_lshl_add_u64 v[214:215], s[26:27], 0, v[130:131]
	s_add_i32 s26, s71, s35
	s_mov_b32 m0, s26
	ds_read_b128 v[182:185], v160 offset:16384
	ds_read_b128 v[186:189], v160 offset:17408
	ds_read_b128 v[190:193], v160 offset:18432
	ds_read_b128 v[194:197], v160 offset:19456
	ds_read_b128 v[198:201], v160 offset:20480
	ds_read_b128 v[202:205], v160 offset:21504
	ds_read_b128 v[206:209], v160 offset:22528
	ds_read_b128 v[210:213], v160 offset:23552
	global_load_lds_dwordx4 v[214:215], off
	v_lshl_add_u64 v[216:217], v[214:215], 0, s[6:7]
	s_add_i32 m0, s26, 0x2000
	s_add_i32 s26, s72, s35
	global_load_lds_dwordx4 v[216:217], off
	v_lshl_add_u64 v[216:217], v[214:215], 0, s[8:9]
	s_mov_b32 m0, s26
	v_lshl_add_u64 v[220:221], s[60:61], 0, v[134:135]
	global_load_lds_dwordx4 v[216:217], off
	v_lshl_add_u64 v[216:217], v[214:215], 0, s[10:11]
	s_add_i32 m0, s26, 0x2000
	s_nop 0
	global_load_lds_dwordx4 v[216:217], off
	v_lshl_add_u64 v[216:217], s[60:61], 0, v[132:133]
	s_mov_b32 m0, s63
	s_nop 0
	global_load_lds_dwordx4 v[216:217], off
	s_mov_b32 m0, s64
	s_nop 0
	global_load_lds_dwordx4 v[220:221], off
	s_waitcnt vmcnt(8)
	s_waitcnt lgkmcnt(0)
	s_barrier
	s_setprio 0
	s_waitcnt lgkmcnt(0)
	v_mfma_f32_16x16x32_bf16 v[62:65], v[144:147], v[182:185], v[62:65]
	v_mfma_f32_16x16x32_bf16 v[58:61], v[152:155], v[182:185], v[58:61]
	v_mfma_f32_16x16x32_bf16 v[54:57], v[144:147], v[190:193], v[54:57]
	v_mfma_f32_16x16x32_bf16 v[46:49], v[152:155], v[190:193], v[46:49]
	v_mfma_f32_16x16x32_bf16 v[38:41], v[144:147], v[198:201], v[38:41]
	v_mfma_f32_16x16x32_bf16 v[30:33], v[152:155], v[198:201], v[30:33]
	v_mfma_f32_16x16x32_bf16 v[22:25], v[144:147], v[206:209], v[22:25]
	v_mfma_f32_16x16x32_bf16 v[14:17], v[152:155], v[206:209], v[14:17]
	v_mfma_f32_16x16x32_bf16 v[62:65], v[148:151], v[186:189], v[62:65]
	v_mfma_f32_16x16x32_bf16 v[58:61], v[162:165], v[186:189], v[58:61]
	v_mfma_f32_16x16x32_bf16 v[54:57], v[148:151], v[194:197], v[54:57]
	v_mfma_f32_16x16x32_bf16 v[46:49], v[162:165], v[194:197], v[46:49]
	v_mfma_f32_16x16x32_bf16 v[38:41], v[148:151], v[202:205], v[38:41]
	v_mfma_f32_16x16x32_bf16 v[30:33], v[162:165], v[202:205], v[30:33]
	v_mfma_f32_16x16x32_bf16 v[22:25], v[148:151], v[210:213], v[22:25]
	v_mfma_f32_16x16x32_bf16 v[14:17], v[162:165], v[210:213], v[14:17]
	v_mfma_f32_16x16x32_bf16 v[50:53], v[166:169], v[182:185], v[50:53]
	v_mfma_f32_16x16x32_bf16 v[42:45], v[174:177], v[182:185], v[42:45]
	v_mfma_f32_16x16x32_bf16 v[34:37], v[166:169], v[190:193], v[34:37]
	v_mfma_f32_16x16x32_bf16 v[26:29], v[174:177], v[190:193], v[26:29]
	v_mfma_f32_16x16x32_bf16 v[18:21], v[166:169], v[198:201], v[18:21]
	v_mfma_f32_16x16x32_bf16 v[10:13], v[174:177], v[198:201], v[10:13]
	v_mfma_f32_16x16x32_bf16 v[6:9], v[166:169], v[206:209], v[6:9]
	v_mfma_f32_16x16x32_bf16 v[2:5], v[174:177], v[206:209], v[2:5]
	v_mfma_f32_16x16x32_bf16 v[50:53], v[170:173], v[186:189], v[50:53]
	v_mfma_f32_16x16x32_bf16 v[42:45], v[178:181], v[186:189], v[42:45]
	v_mfma_f32_16x16x32_bf16 v[34:37], v[170:173], v[194:197], v[34:37]
	v_mfma_f32_16x16x32_bf16 v[26:29], v[178:181], v[194:197], v[26:29]
	v_mfma_f32_16x16x32_bf16 v[18:21], v[170:173], v[202:205], v[18:21]
	v_mfma_f32_16x16x32_bf16 v[10:13], v[178:181], v[202:205], v[10:13]
	v_mfma_f32_16x16x32_bf16 v[6:9], v[170:173], v[210:213], v[6:9]
	v_mfma_f32_16x16x32_bf16 v[2:5], v[178:181], v[210:213], v[2:5]
	s_setprio 1
	s_barrier
	s_add_i32 s81, 0, 0x18000
	v_add_u32_e32 v161, s81, v156
	s_add_i32 s82, 0, 0x1c000
	ds_read_b128 v[144:147], v161
	ds_read_b128 v[148:151], v161 offset:1024
	ds_read_b128 v[152:155], v161 offset:2048
	ds_read_b128 v[162:165], v161 offset:3072
	v_add_u32_e32 v161, s82, v156
	ds_read_b128 v[166:169], v161
	ds_read_b128 v[170:173], v161 offset:1024
	ds_read_b128 v[174:177], v161 offset:2048
	ds_read_b128 v[178:181], v161 offset:3072
	s_add_u32 s26, s60, 0x80000
	s_addc_u32 s27, s61, 0
	s_mov_b32 m0, s65
	v_lshl_add_u64 v[222:223], s[26:27], 0, v[132:133]
	ds_read_b128 v[182:185], v160 offset:32768
	ds_read_b128 v[186:189], v160 offset:33792
	ds_read_b128 v[190:193], v160 offset:34816
	ds_read_b128 v[194:197], v160 offset:35840
	ds_read_b128 v[198:201], v160 offset:36864
	ds_read_b128 v[202:205], v160 offset:37888
	ds_read_b128 v[206:209], v160 offset:38912
	ds_read_b128 v[210:213], v160 offset:39936
	global_load_lds_dwordx4 v[222:223], off
	v_lshl_add_u64 v[222:223], s[26:27], 0, v[134:135]
	s_mov_b32 m0, s66
	s_nop 0
	global_load_lds_dwordx4 v[222:223], off
	s_waitcnt vmcnt(8)
	s_waitcnt lgkmcnt(0)
	s_barrier
	s_setprio 0
	s_waitcnt lgkmcnt(0)
	v_mfma_f32_16x16x32_bf16 v[126:129], v[144:147], v[182:185], v[126:129]
	v_mfma_f32_16x16x32_bf16 v[122:125], v[152:155], v[182:185], v[122:125]
	v_mfma_f32_16x16x32_bf16 v[118:121], v[144:147], v[190:193], v[118:121]
	v_mfma_f32_16x16x32_bf16 v[114:117], v[152:155], v[190:193], v[114:117]
	v_mfma_f32_16x16x32_bf16 v[106:109], v[144:147], v[198:201], v[106:109]
	v_mfma_f32_16x16x32_bf16 v[98:101], v[152:155], v[198:201], v[98:101]
	v_mfma_f32_16x16x32_bf16 v[90:93], v[144:147], v[206:209], v[90:93]
	v_mfma_f32_16x16x32_bf16 v[82:85], v[152:155], v[206:209], v[82:85]
	v_mfma_f32_16x16x32_bf16 v[126:129], v[148:151], v[186:189], v[126:129]
	v_mfma_f32_16x16x32_bf16 v[122:125], v[162:165], v[186:189], v[122:125]
	v_mfma_f32_16x16x32_bf16 v[118:121], v[148:151], v[194:197], v[118:121]
	v_mfma_f32_16x16x32_bf16 v[114:117], v[162:165], v[194:197], v[114:117]
	v_mfma_f32_16x16x32_bf16 v[106:109], v[148:151], v[202:205], v[106:109]
	v_mfma_f32_16x16x32_bf16 v[98:101], v[162:165], v[202:205], v[98:101]
	v_mfma_f32_16x16x32_bf16 v[90:93], v[148:151], v[210:213], v[90:93]
	v_mfma_f32_16x16x32_bf16 v[82:85], v[162:165], v[210:213], v[82:85]
	v_mfma_f32_16x16x32_bf16 v[110:113], v[166:169], v[182:185], v[110:113]
	v_mfma_f32_16x16x32_bf16 v[102:105], v[174:177], v[182:185], v[102:105]
	v_mfma_f32_16x16x32_bf16 v[94:97], v[166:169], v[190:193], v[94:97]
	v_mfma_f32_16x16x32_bf16 v[86:89], v[174:177], v[190:193], v[86:89]
	v_mfma_f32_16x16x32_bf16 v[78:81], v[166:169], v[198:201], v[78:81]
	v_mfma_f32_16x16x32_bf16 v[74:77], v[174:177], v[198:201], v[74:77]
	v_mfma_f32_16x16x32_bf16 v[70:73], v[166:169], v[206:209], v[70:73]
	v_mfma_f32_16x16x32_bf16 v[66:69], v[174:177], v[206:209], v[66:69]
	v_mfma_f32_16x16x32_bf16 v[110:113], v[170:173], v[186:189], v[110:113]
	v_mfma_f32_16x16x32_bf16 v[102:105], v[178:181], v[186:189], v[102:105]
	v_mfma_f32_16x16x32_bf16 v[94:97], v[170:173], v[194:197], v[94:97]
	v_mfma_f32_16x16x32_bf16 v[86:89], v[178:181], v[194:197], v[86:89]
	v_mfma_f32_16x16x32_bf16 v[78:81], v[170:173], v[202:205], v[78:81]
	v_mfma_f32_16x16x32_bf16 v[74:77], v[178:181], v[202:205], v[74:77]
	v_mfma_f32_16x16x32_bf16 v[70:73], v[170:173], v[210:213], v[70:73]
	v_mfma_f32_16x16x32_bf16 v[66:69], v[178:181], v[210:213], v[66:69]
	s_setprio 1
	s_barrier
	s_add_i32 s26, s81, s35
	v_lshl_add_u64 v[222:223], v[214:215], 0, s[14:15]
	s_mov_b32 m0, s26
	ds_read_b128 v[182:185], v160 offset:49152
	ds_read_b128 v[186:189], v160 offset:50176
	ds_read_b128 v[190:193], v160 offset:51200
	ds_read_b128 v[194:197], v160 offset:52224
	ds_read_b128 v[198:201], v160 offset:53248
	ds_read_b128 v[202:205], v160 offset:54272
	ds_read_b128 v[206:209], v160 offset:55296
	ds_read_b128 v[210:213], v160 offset:56320
	global_load_lds_dwordx4 v[222:223], off
	v_lshl_add_u64 v[222:223], v[214:215], 0, s[16:17]
	s_add_i32 m0, s26, 0x2000
	s_add_i32 s26, s82, s35
	global_load_lds_dwordx4 v[222:223], off
	v_lshl_add_u64 v[222:223], v[214:215], 0, s[20:21]
	s_mov_b32 m0, s26
	v_lshl_add_u64 v[214:215], v[214:215], 0, s[22:23]
	global_load_lds_dwordx4 v[222:223], off
	s_add_i32 m0, s26, 0x2000
	s_nop 0
	global_load_lds_dwordx4 v[214:215], off
	v_lshl_add_u64 v[214:215], v[216:217], 0, s[18:19]
	s_mov_b32 m0, s68
	s_nop 0
	global_load_lds_dwordx4 v[214:215], off
	v_lshl_add_u64 v[214:215], v[220:221], 0, s[18:19]
	s_mov_b32 m0, s69
	s_nop 0
	global_load_lds_dwordx4 v[214:215], off
	s_waitcnt vmcnt(8)
	s_waitcnt lgkmcnt(0)
	s_barrier
	s_setprio 0
	s_waitcnt lgkmcnt(0)
	v_mfma_f32_16x16x32_bf16 v[62:65], v[144:147], v[182:185], v[62:65]
	v_mfma_f32_16x16x32_bf16 v[58:61], v[152:155], v[182:185], v[58:61]
	v_mfma_f32_16x16x32_bf16 v[54:57], v[144:147], v[190:193], v[54:57]
	v_mfma_f32_16x16x32_bf16 v[46:49], v[152:155], v[190:193], v[46:49]
	v_mfma_f32_16x16x32_bf16 v[38:41], v[144:147], v[198:201], v[38:41]
	v_mfma_f32_16x16x32_bf16 v[30:33], v[152:155], v[198:201], v[30:33]
	v_mfma_f32_16x16x32_bf16 v[22:25], v[144:147], v[206:209], v[22:25]
	v_mfma_f32_16x16x32_bf16 v[14:17], v[152:155], v[206:209], v[14:17]
	v_mfma_f32_16x16x32_bf16 v[62:65], v[148:151], v[186:189], v[62:65]
	v_mfma_f32_16x16x32_bf16 v[58:61], v[162:165], v[186:189], v[58:61]
	v_mfma_f32_16x16x32_bf16 v[54:57], v[148:151], v[194:197], v[54:57]
	v_mfma_f32_16x16x32_bf16 v[46:49], v[162:165], v[194:197], v[46:49]
	v_mfma_f32_16x16x32_bf16 v[38:41], v[148:151], v[202:205], v[38:41]
	v_mfma_f32_16x16x32_bf16 v[30:33], v[162:165], v[202:205], v[30:33]
	v_mfma_f32_16x16x32_bf16 v[22:25], v[148:151], v[210:213], v[22:25]
	v_mfma_f32_16x16x32_bf16 v[14:17], v[162:165], v[210:213], v[14:17]
	v_mfma_f32_16x16x32_bf16 v[50:53], v[166:169], v[182:185], v[50:53]
	v_mfma_f32_16x16x32_bf16 v[42:45], v[174:177], v[182:185], v[42:45]
	v_mfma_f32_16x16x32_bf16 v[34:37], v[166:169], v[190:193], v[34:37]
	v_mfma_f32_16x16x32_bf16 v[26:29], v[174:177], v[190:193], v[26:29]
	v_mfma_f32_16x16x32_bf16 v[18:21], v[166:169], v[198:201], v[18:21]
	v_mfma_f32_16x16x32_bf16 v[10:13], v[174:177], v[198:201], v[10:13]
	v_mfma_f32_16x16x32_bf16 v[6:9], v[166:169], v[206:209], v[6:9]
	v_mfma_f32_16x16x32_bf16 v[2:5], v[174:177], v[206:209], v[2:5]
	v_mfma_f32_16x16x32_bf16 v[50:53], v[170:173], v[186:189], v[50:53]
	v_mfma_f32_16x16x32_bf16 v[42:45], v[178:181], v[186:189], v[42:45]
	v_mfma_f32_16x16x32_bf16 v[34:37], v[170:173], v[194:197], v[34:37]
	v_mfma_f32_16x16x32_bf16 v[26:29], v[178:181], v[194:197], v[26:29]
	v_mfma_f32_16x16x32_bf16 v[18:21], v[170:173], v[202:205], v[18:21]
	v_mfma_f32_16x16x32_bf16 v[10:13], v[178:181], v[202:205], v[10:13]
	v_mfma_f32_16x16x32_bf16 v[6:9], v[170:173], v[210:213], v[6:9]
	v_mfma_f32_16x16x32_bf16 v[2:5], v[178:181], v[210:213], v[2:5]
	s_setprio 1
	s_barrier
	s_add_i32 s80, s80, 2
	s_add_u32 s74, s74, 0x10000
	s_addc_u32 s75, s75, 0
	s_add_u32 s58, s58, 0x100
	s_addc_u32 s59, s59, 0
	s_cmp_gt_u32 s80, 29
	s_cbranch_scc0 .LBB0_1271
	s_and_b64 vcc, exec, s[24:25]
	s_cbranch_vccz .LBB0_1274
	s_barrier

.LBB0_1497:
	ds_read_b128 v[26:29], v186
	ds_read_b128 v[30:33], v186 offset:1024
	ds_read_b128 v[18:21], v186 offset:2048
	ds_read_b128 v[22:25], v186 offset:3072
	ds_read_b128 v[10:13], v187
	ds_read_b128 v[14:17], v187 offset:1024
	ds_read_b128 v[2:5], v187 offset:2048
	ds_read_b128 v[6:9], v187 offset:3072
	s_add_u32 s56, s4, 0xfffc0080
	s_addc_u32 s57, s5, -1
	s_cmp_eq_u32 s49, 12
	s_cselect_b64 vcc, -1, 0
	s_cselect_b32 s57, s2, s57
	s_cselect_b32 s56, s47, s56
	v_cndmask_b32_e32 v179, v177, v175, vcc
	v_cndmask_b32_e32 v178, v176, v174, vcc
	v_lshl_add_u64 v[180:181], s[4:5], 0, v[168:169]
	s_add_i32 m0, s62, 0xc000
	ds_read_b128 v[192:195], v188
	ds_read_b128 v[196:199], v188 offset:1024
	ds_read_b128 v[200:203], v188 offset:2048
	ds_read_b128 v[204:207], v188 offset:3072
	ds_read_b128 v[208:211], v188 offset:4096
	ds_read_b128 v[212:215], v188 offset:5120
	ds_read_b128 v[220:223], v188 offset:6144
	ds_read_b128 v[224:227], v188 offset:7168
	global_load_lds_dwordx4 v[180:181], off
	v_lshl_add_u64 v[180:181], s[4:5], 0, v[170:171]
	s_add_i32 m0, s62, 0xe000
	s_nop 0
	global_load_lds_dwordx4 v[180:181], off
	s_waitcnt vmcnt(8)
	s_waitcnt lgkmcnt(0)
	s_barrier
	s_setprio 0
	s_waitcnt lgkmcnt(0)
	v_mfma_scale_f32_16x16x128_f8f6f4 v[158:161], v[26:33], v[192:199], v[158:161], v189, v190 op_sel_hi:[0,0,0]
	v_mfma_scale_f32_16x16x128_f8f6f4 v[150:153], v[18:25], v[192:199], v[150:153], v189, v190 op_sel_hi:[0,0,0]
	v_mfma_scale_f32_16x16x128_f8f6f4 v[142:145], v[26:33], v[200:207], v[142:145], v189, v190 op_sel_hi:[0,0,0]
	v_mfma_scale_f32_16x16x128_f8f6f4 v[134:137], v[18:25], v[200:207], v[134:137], v189, v190 op_sel_hi:[0,0,0]
	v_mfma_scale_f32_16x16x128_f8f6f4 v[126:129], v[26:33], v[208:215], v[126:129], v189, v190 op_sel_hi:[0,0,0]
	v_mfma_scale_f32_16x16x128_f8f6f4 v[118:121], v[18:25], v[208:215], v[118:121], v189, v190 op_sel_hi:[0,0,0]
	v_mfma_scale_f32_16x16x128_f8f6f4 v[110:113], v[26:33], v[220:227], v[110:113], v189, v190 op_sel_hi:[0,0,0]
	v_mfma_scale_f32_16x16x128_f8f6f4 v[102:105], v[18:25], v[220:227], v[102:105], v189, v190 op_sel_hi:[0,0,0]
	v_mfma_scale_f32_16x16x128_f8f6f4 v[154:157], v[10:17], v[192:199], v[154:157], v189, v190 op_sel_hi:[0,0,0]
	v_mfma_scale_f32_16x16x128_f8f6f4 v[146:149], v[2:9], v[192:199], v[146:149], v189, v190 op_sel_hi:[0,0,0]
	v_mfma_scale_f32_16x16x128_f8f6f4 v[138:141], v[10:17], v[200:207], v[138:141], v189, v190 op_sel_hi:[0,0,0]
	v_mfma_scale_f32_16x16x128_f8f6f4 v[130:133], v[2:9], v[200:207], v[130:133], v189, v190 op_sel_hi:[0,0,0]
	v_mfma_scale_f32_16x16x128_f8f6f4 v[122:125], v[10:17], v[208:215], v[122:125], v189, v190 op_sel_hi:[0,0,0]
	v_mfma_scale_f32_16x16x128_f8f6f4 v[114:117], v[2:9], v[208:215], v[114:117], v189, v190 op_sel_hi:[0,0,0]
	v_mfma_scale_f32_16x16x128_f8f6f4 v[106:109], v[10:17], v[220:227], v[106:109], v189, v190 op_sel_hi:[0,0,0]
	v_mfma_scale_f32_16x16x128_f8f6f4 v[98:101], v[2:9], v[220:227], v[98:101], v189, v190 op_sel_hi:[0,0,0]
	s_setprio 1
	s_barrier
	s_add_i32 s73, s69, s61
	v_lshl_add_u64 v[178:179], v[178:179], 0, v[162:163]
	s_mov_b32 m0, s73
	ds_read_b128 v[192:195], v188 offset:16384
	ds_read_b128 v[196:199], v188 offset:17408
	ds_read_b128 v[200:203], v188 offset:18432
	ds_read_b128 v[204:207], v188 offset:19456
	ds_read_b128 v[208:211], v188 offset:20480
	ds_read_b128 v[212:215], v188 offset:21504
	ds_read_b128 v[220:223], v188 offset:22528
	ds_read_b128 v[224:227], v188 offset:23552
	global_load_lds_dwordx4 v[178:179], off
	v_lshl_add_u64 v[180:181], v[178:179], 0, s[10:11]
	s_add_i32 m0, s73, 0x2000
	s_add_i32 s73, s70, s61
	global_load_lds_dwordx4 v[180:181], off
	v_lshl_add_u64 v[180:181], v[178:179], 0, s[12:13]
	s_mov_b32 m0, s73
	v_lshl_add_u64 v[182:183], s[56:57], 0, v[166:167]
	global_load_lds_dwordx4 v[180:181], off
	v_lshl_add_u64 v[180:181], v[178:179], 0, s[14:15]
	s_add_i32 m0, s73, 0x2000
	s_nop 0
	global_load_lds_dwordx4 v[180:181], off
	v_lshl_add_u64 v[180:181], s[56:57], 0, v[164:165]
	s_mov_b32 m0, s62
	s_nop 0
	global_load_lds_dwordx4 v[180:181], off
	s_mov_b32 m0, s53
	s_nop 0
	global_load_lds_dwordx4 v[182:183], off
	s_waitcnt vmcnt(8)
	s_waitcnt lgkmcnt(0)
	s_barrier
	s_setprio 0
	s_waitcnt lgkmcnt(0)
	v_mfma_scale_f32_16x16x128_f8f6f4 v[94:97], v[26:33], v[192:199], v[94:97], v189, v190 op_sel_hi:[0,0,0]
	v_mfma_scale_f32_16x16x128_f8f6f4 v[86:89], v[18:25], v[192:199], v[86:89], v189, v190 op_sel_hi:[0,0,0]
	v_mfma_scale_f32_16x16x128_f8f6f4 v[78:81], v[26:33], v[200:207], v[78:81], v189, v190 op_sel_hi:[0,0,0]
	v_mfma_scale_f32_16x16x128_f8f6f4 v[70:73], v[18:25], v[200:207], v[70:73], v189, v190 op_sel_hi:[0,0,0]
	v_mfma_scale_f32_16x16x128_f8f6f4 v[62:65], v[26:33], v[208:215], v[62:65], v189, v190 op_sel_hi:[0,0,0]
	v_mfma_scale_f32_16x16x128_f8f6f4 v[54:57], v[18:25], v[208:215], v[54:57], v189, v190 op_sel_hi:[0,0,0]
	v_mfma_scale_f32_16x16x128_f8f6f4 v[46:49], v[26:33], v[220:227], v[46:49], v189, v190 op_sel_hi:[0,0,0]
	v_mfma_scale_f32_16x16x128_f8f6f4 v[38:41], v[18:25], v[220:227], v[38:41], v189, v190 op_sel_hi:[0,0,0]
	v_mfma_scale_f32_16x16x128_f8f6f4 v[90:93], v[10:17], v[192:199], v[90:93], v189, v190 op_sel_hi:[0,0,0]
	v_mfma_scale_f32_16x16x128_f8f6f4 v[82:85], v[2:9], v[192:199], v[82:85], v189, v190 op_sel_hi:[0,0,0]
	v_mfma_scale_f32_16x16x128_f8f6f4 v[74:77], v[10:17], v[200:207], v[74:77], v189, v190 op_sel_hi:[0,0,0]
	v_mfma_scale_f32_16x16x128_f8f6f4 v[66:69], v[2:9], v[200:207], v[66:69], v189, v190 op_sel_hi:[0,0,0]
	v_mfma_scale_f32_16x16x128_f8f6f4 v[58:61], v[10:17], v[208:215], v[58:61], v189, v190 op_sel_hi:[0,0,0]
	v_mfma_scale_f32_16x16x128_f8f6f4 v[50:53], v[2:9], v[208:215], v[50:53], v189, v190 op_sel_hi:[0,0,0]
	v_mfma_scale_f32_16x16x128_f8f6f4 v[42:45], v[10:17], v[220:227], v[42:45], v189, v190 op_sel_hi:[0,0,0]
	v_mfma_scale_f32_16x16x128_f8f6f4 v[34:37], v[2:9], v[220:227], v[34:37], v189, v190 op_sel_hi:[0,0,0]
	s_setprio 1
	s_barrier
	s_add_i32 s73, 0, 0x18000
	s_add_i32 s74, 0, 0x1c000
	v_add_u32_e32 v14, s73, v184
	v_add_u32_e32 v30, s74, v184
	ds_read_b128 v[2:5], v14
	ds_read_b128 v[6:9], v14 offset:1024
	ds_read_b128 v[10:13], v14 offset:2048
	ds_read_b128 v[14:17], v14 offset:3072
	ds_read_b128 v[18:21], v30
	ds_read_b128 v[22:25], v30 offset:1024
	ds_read_b128 v[26:29], v30 offset:2048
	ds_read_b128 v[30:33], v30 offset:3072
	s_add_u32 s56, s56, 0x40000
	s_addc_u32 s57, s57, 0
	s_mov_b32 m0, s63
	v_lshl_add_u64 v[216:217], s[56:57], 0, v[164:165]
	ds_read_b128 v[192:195], v188 offset:32768
	ds_read_b128 v[196:199], v188 offset:33792
	ds_read_b128 v[200:203], v188 offset:34816
	ds_read_b128 v[204:207], v188 offset:35840
	ds_read_b128 v[208:211], v188 offset:36864
	ds_read_b128 v[212:215], v188 offset:37888
	ds_read_b128 v[220:223], v188 offset:38912
	ds_read_b128 v[224:227], v188 offset:39936
	global_load_lds_dwordx4 v[216:217], off
	v_lshl_add_u64 v[216:217], s[56:57], 0, v[166:167]
	s_mov_b32 m0, s64
	s_nop 0
	global_load_lds_dwordx4 v[216:217], off
	s_waitcnt vmcnt(8)
	s_waitcnt lgkmcnt(0)
	s_barrier
	s_setprio 0
	s_waitcnt lgkmcnt(0)
	v_mfma_scale_f32_16x16x128_f8f6f4 v[158:161], v[2:9], v[192:199], v[158:161], v189, v190 op_sel_hi:[0,0,0]
	v_mfma_scale_f32_16x16x128_f8f6f4 v[150:153], v[10:17], v[192:199], v[150:153], v189, v190 op_sel_hi:[0,0,0]
	v_mfma_scale_f32_16x16x128_f8f6f4 v[142:145], v[2:9], v[200:207], v[142:145], v189, v190 op_sel_hi:[0,0,0]
	v_mfma_scale_f32_16x16x128_f8f6f4 v[134:137], v[10:17], v[200:207], v[134:137], v189, v190 op_sel_hi:[0,0,0]
	v_mfma_scale_f32_16x16x128_f8f6f4 v[126:129], v[2:9], v[208:215], v[126:129], v189, v190 op_sel_hi:[0,0,0]
	v_mfma_scale_f32_16x16x128_f8f6f4 v[118:121], v[10:17], v[208:215], v[118:121], v189, v190 op_sel_hi:[0,0,0]
	v_mfma_scale_f32_16x16x128_f8f6f4 v[110:113], v[2:9], v[220:227], v[110:113], v189, v190 op_sel_hi:[0,0,0]
	v_mfma_scale_f32_16x16x128_f8f6f4 v[102:105], v[10:17], v[220:227], v[102:105], v189, v190 op_sel_hi:[0,0,0]
	v_mfma_scale_f32_16x16x128_f8f6f4 v[154:157], v[18:25], v[192:199], v[154:157], v189, v190 op_sel_hi:[0,0,0]
	v_mfma_scale_f32_16x16x128_f8f6f4 v[146:149], v[26:33], v[192:199], v[146:149], v189, v190 op_sel_hi:[0,0,0]
	v_mfma_scale_f32_16x16x128_f8f6f4 v[138:141], v[18:25], v[200:207], v[138:141], v189, v190 op_sel_hi:[0,0,0]
	v_mfma_scale_f32_16x16x128_f8f6f4 v[130:133], v[26:33], v[200:207], v[130:133], v189, v190 op_sel_hi:[0,0,0]
	v_mfma_scale_f32_16x16x128_f8f6f4 v[122:125], v[18:25], v[208:215], v[122:125], v189, v190 op_sel_hi:[0,0,0]
	v_mfma_scale_f32_16x16x128_f8f6f4 v[114:117], v[26:33], v[208:215], v[114:117], v189, v190 op_sel_hi:[0,0,0]
	v_mfma_scale_f32_16x16x128_f8f6f4 v[106:109], v[18:25], v[220:227], v[106:109], v189, v190 op_sel_hi:[0,0,0]
	v_mfma_scale_f32_16x16x128_f8f6f4 v[98:101], v[26:33], v[220:227], v[98:101], v189, v190 op_sel_hi:[0,0,0]
	s_setprio 1
	s_barrier
	s_add_i32 s56, s73, s61
	v_lshl_add_u64 v[216:217], v[178:179], 0, s[20:21]
	s_mov_b32 m0, s56
	ds_read_b128 v[192:195], v188 offset:49152
	ds_read_b128 v[196:199], v188 offset:50176
	ds_read_b128 v[200:203], v188 offset:51200
	ds_read_b128 v[204:207], v188 offset:52224
	ds_read_b128 v[208:211], v188 offset:53248
	ds_read_b128 v[212:215], v188 offset:54272
	ds_read_b128 v[220:223], v188 offset:55296
	ds_read_b128 v[224:227], v188 offset:56320
	global_load_lds_dwordx4 v[216:217], off
	v_lshl_add_u64 v[216:217], v[178:179], 0, s[22:23]
	s_add_i32 m0, s56, 0x2000
	s_add_i32 s56, s74, s61
	global_load_lds_dwordx4 v[216:217], off
	v_lshl_add_u64 v[216:217], v[178:179], 0, s[26:27]
	s_mov_b32 m0, s56
	v_lshl_add_u64 v[178:179], v[178:179], 0, s[36:37]
	global_load_lds_dwordx4 v[216:217], off
	s_add_i32 m0, s56, 0x2000
	s_nop 0
	global_load_lds_dwordx4 v[178:179], off
	v_lshl_add_u64 v[178:179], v[180:181], 0, s[24:25]
	s_mov_b32 m0, s66
	s_nop 0
	global_load_lds_dwordx4 v[178:179], off
	v_lshl_add_u64 v[178:179], v[182:183], 0, s[24:25]
	s_mov_b32 m0, s67
	s_nop 0
	global_load_lds_dwordx4 v[178:179], off
	s_waitcnt vmcnt(8)
	s_waitcnt lgkmcnt(0)
	s_barrier
	s_setprio 0
	s_waitcnt lgkmcnt(0)
	v_mfma_scale_f32_16x16x128_f8f6f4 v[94:97], v[2:9], v[192:199], v[94:97], v189, v190 op_sel_hi:[0,0,0]
	v_mfma_scale_f32_16x16x128_f8f6f4 v[86:89], v[10:17], v[192:199], v[86:89], v189, v190 op_sel_hi:[0,0,0]
	v_mfma_scale_f32_16x16x128_f8f6f4 v[78:81], v[2:9], v[200:207], v[78:81], v189, v190 op_sel_hi:[0,0,0]
	v_mfma_scale_f32_16x16x128_f8f6f4 v[70:73], v[10:17], v[200:207], v[70:73], v189, v190 op_sel_hi:[0,0,0]
	v_mfma_scale_f32_16x16x128_f8f6f4 v[62:65], v[2:9], v[208:215], v[62:65], v189, v190 op_sel_hi:[0,0,0]
	v_mfma_scale_f32_16x16x128_f8f6f4 v[54:57], v[10:17], v[208:215], v[54:57], v189, v190 op_sel_hi:[0,0,0]
	v_mfma_scale_f32_16x16x128_f8f6f4 v[46:49], v[2:9], v[220:227], v[46:49], v189, v190 op_sel_hi:[0,0,0]
	v_mfma_scale_f32_16x16x128_f8f6f4 v[38:41], v[10:17], v[220:227], v[38:41], v189, v190 op_sel_hi:[0,0,0]
	v_mfma_scale_f32_16x16x128_f8f6f4 v[90:93], v[18:25], v[192:199], v[90:93], v189, v190 op_sel_hi:[0,0,0]
	v_mfma_scale_f32_16x16x128_f8f6f4 v[82:85], v[26:33], v[192:199], v[82:85], v189, v190 op_sel_hi:[0,0,0]
	v_mfma_scale_f32_16x16x128_f8f6f4 v[74:77], v[18:25], v[200:207], v[74:77], v189, v190 op_sel_hi:[0,0,0]
	v_mfma_scale_f32_16x16x128_f8f6f4 v[66:69], v[26:33], v[200:207], v[66:69], v189, v190 op_sel_hi:[0,0,0]
	v_mfma_scale_f32_16x16x128_f8f6f4 v[58:61], v[18:25], v[208:215], v[58:61], v189, v190 op_sel_hi:[0,0,0]
	v_mfma_scale_f32_16x16x128_f8f6f4 v[50:53], v[26:33], v[208:215], v[50:53], v189, v190 op_sel_hi:[0,0,0]
	v_mfma_scale_f32_16x16x128_f8f6f4 v[42:45], v[18:25], v[220:227], v[42:45], v189, v190 op_sel_hi:[0,0,0]
	v_mfma_scale_f32_16x16x128_f8f6f4 v[34:37], v[26:33], v[220:227], v[34:37], v189, v190 op_sel_hi:[0,0,0]
	s_setprio 1
	s_barrier
	s_add_i32 s49, s49, 2
	s_add_u32 s4, s4, 0x100
	s_addc_u32 s5, s5, 0
	s_cmp_gt_u32 s49, 13
	v_lshl_add_u64 v[176:177], v[176:177], 0, s[40:41]
	s_cbranch_scc0 .LBB0_1497
	s_and_b64 vcc, exec, s[38:39]
	s_cbranch_vccz .LBB0_1500
	s_barrier

.LBB0_1568:
	ds_read_b128 v[26:29], v186
	ds_read_b128 v[30:33], v186 offset:1024
	ds_read_b128 v[18:21], v186 offset:2048
	ds_read_b128 v[22:25], v186 offset:3072
	ds_read_b128 v[10:13], v187
	ds_read_b128 v[14:17], v187 offset:1024
	ds_read_b128 v[2:5], v187 offset:2048
	ds_read_b128 v[6:9], v187 offset:3072
	s_add_u32 s58, s56, 0xfff50080
	s_addc_u32 s59, s57, -1
	s_cmp_eq_u32 s53, 40
	s_cselect_b64 vcc, -1, 0
	s_cselect_b32 s59, s5, s59
	s_cselect_b32 s58, s4, s58
	v_cndmask_b32_e32 v179, v177, v175, vcc
	v_cndmask_b32_e32 v178, v176, v174, vcc
	v_lshl_add_u64 v[180:181], s[56:57], 0, v[170:171]
	s_add_i32 m0, s61, 0xc000
	ds_read_b128 v[192:195], v188
	ds_read_b128 v[196:199], v188 offset:1024
	ds_read_b128 v[200:203], v188 offset:2048
	ds_read_b128 v[204:207], v188 offset:3072
	ds_read_b128 v[208:211], v188 offset:4096
	ds_read_b128 v[212:215], v188 offset:5120
	ds_read_b128 v[220:223], v188 offset:6144
	ds_read_b128 v[224:227], v188 offset:7168
	global_load_lds_dwordx4 v[180:181], off
	v_lshl_add_u64 v[180:181], s[56:57], 0, v[172:173]
	s_add_i32 m0, s61, 0xe000
	s_nop 0
	global_load_lds_dwordx4 v[180:181], off
	s_waitcnt vmcnt(8)
	s_waitcnt lgkmcnt(0)
	s_barrier
	s_setprio 0
	s_waitcnt lgkmcnt(0)
	v_mfma_scale_f32_16x16x128_f8f6f4 v[158:161], v[26:33], v[192:199], v[158:161], v189, v190 op_sel_hi:[0,0,0]
	v_mfma_scale_f32_16x16x128_f8f6f4 v[154:157], v[18:25], v[192:199], v[154:157], v189, v190 op_sel_hi:[0,0,0]
	v_mfma_scale_f32_16x16x128_f8f6f4 v[150:153], v[26:33], v[200:207], v[150:153], v189, v190 op_sel_hi:[0,0,0]
	v_mfma_scale_f32_16x16x128_f8f6f4 v[142:145], v[18:25], v[200:207], v[142:145], v189, v190 op_sel_hi:[0,0,0]
	v_mfma_scale_f32_16x16x128_f8f6f4 v[134:137], v[26:33], v[208:215], v[134:137], v189, v190 op_sel_hi:[0,0,0]
	v_mfma_scale_f32_16x16x128_f8f6f4 v[126:129], v[18:25], v[208:215], v[126:129], v189, v190 op_sel_hi:[0,0,0]
	v_mfma_scale_f32_16x16x128_f8f6f4 v[118:121], v[26:33], v[220:227], v[118:121], v189, v190 op_sel_hi:[0,0,0]
	v_mfma_scale_f32_16x16x128_f8f6f4 v[110:113], v[18:25], v[220:227], v[110:113], v189, v190 op_sel_hi:[0,0,0]
	v_mfma_scale_f32_16x16x128_f8f6f4 v[146:149], v[10:17], v[192:199], v[146:149], v189, v190 op_sel_hi:[0,0,0]
	v_mfma_scale_f32_16x16x128_f8f6f4 v[138:141], v[2:9], v[192:199], v[138:141], v189, v190 op_sel_hi:[0,0,0]
	v_mfma_scale_f32_16x16x128_f8f6f4 v[130:133], v[10:17], v[200:207], v[130:133], v189, v190 op_sel_hi:[0,0,0]
	v_mfma_scale_f32_16x16x128_f8f6f4 v[122:125], v[2:9], v[200:207], v[122:125], v189, v190 op_sel_hi:[0,0,0]
	v_mfma_scale_f32_16x16x128_f8f6f4 v[114:117], v[10:17], v[208:215], v[114:117], v189, v190 op_sel_hi:[0,0,0]
	v_mfma_scale_f32_16x16x128_f8f6f4 v[106:109], v[2:9], v[208:215], v[106:109], v189, v190 op_sel_hi:[0,0,0]
	v_mfma_scale_f32_16x16x128_f8f6f4 v[102:105], v[10:17], v[220:227], v[102:105], v189, v190 op_sel_hi:[0,0,0]
	v_mfma_scale_f32_16x16x128_f8f6f4 v[98:101], v[2:9], v[220:227], v[98:101], v189, v190 op_sel_hi:[0,0,0]
	s_setprio 1
	s_barrier
	s_add_i32 s80, s69, s33
	v_lshl_add_u64 v[178:179], v[178:179], 0, v[164:165]
	s_mov_b32 m0, s80
	ds_read_b128 v[192:195], v188 offset:16384
	ds_read_b128 v[196:199], v188 offset:17408
	ds_read_b128 v[200:203], v188 offset:18432
	ds_read_b128 v[204:207], v188 offset:19456
	ds_read_b128 v[208:211], v188 offset:20480
	ds_read_b128 v[212:215], v188 offset:21504
	ds_read_b128 v[220:223], v188 offset:22528
	ds_read_b128 v[224:227], v188 offset:23552
	global_load_lds_dwordx4 v[178:179], off
	v_lshl_add_u64 v[180:181], v[178:179], 0, s[10:11]
	s_add_i32 m0, s80, 0x2000
	s_add_i32 s80, s70, s33
	global_load_lds_dwordx4 v[180:181], off
	v_lshl_add_u64 v[180:181], v[178:179], 0, s[12:13]
	s_mov_b32 m0, s80
	v_lshl_add_u64 v[182:183], s[58:59], 0, v[168:169]
	global_load_lds_dwordx4 v[180:181], off
	v_lshl_add_u64 v[180:181], v[178:179], 0, s[14:15]
	s_add_i32 m0, s80, 0x2000
	s_nop 0
	global_load_lds_dwordx4 v[180:181], off
	v_lshl_add_u64 v[180:181], s[58:59], 0, v[166:167]
	s_mov_b32 m0, s61
	s_nop 0
	global_load_lds_dwordx4 v[180:181], off
	s_mov_b32 m0, s62
	s_nop 0
	global_load_lds_dwordx4 v[182:183], off
	s_waitcnt vmcnt(8)
	s_waitcnt lgkmcnt(0)
	s_barrier
	s_setprio 0
	s_waitcnt lgkmcnt(0)
	v_mfma_scale_f32_16x16x128_f8f6f4 v[94:97], v[26:33], v[192:199], v[94:97], v189, v190 op_sel_hi:[0,0,0]
	v_mfma_scale_f32_16x16x128_f8f6f4 v[90:93], v[18:25], v[192:199], v[90:93], v189, v190 op_sel_hi:[0,0,0]
	v_mfma_scale_f32_16x16x128_f8f6f4 v[86:89], v[26:33], v[200:207], v[86:89], v189, v190 op_sel_hi:[0,0,0]
	v_mfma_scale_f32_16x16x128_f8f6f4 v[78:81], v[18:25], v[200:207], v[78:81], v189, v190 op_sel_hi:[0,0,0]
	v_mfma_scale_f32_16x16x128_f8f6f4 v[70:73], v[26:33], v[208:215], v[70:73], v189, v190 op_sel_hi:[0,0,0]
	v_mfma_scale_f32_16x16x128_f8f6f4 v[62:65], v[18:25], v[208:215], v[62:65], v189, v190 op_sel_hi:[0,0,0]
	v_mfma_scale_f32_16x16x128_f8f6f4 v[54:57], v[26:33], v[220:227], v[54:57], v189, v190 op_sel_hi:[0,0,0]
	v_mfma_scale_f32_16x16x128_f8f6f4 v[46:49], v[18:25], v[220:227], v[46:49], v189, v190 op_sel_hi:[0,0,0]
	v_mfma_scale_f32_16x16x128_f8f6f4 v[82:85], v[10:17], v[192:199], v[82:85], v189, v190 op_sel_hi:[0,0,0]
	v_mfma_scale_f32_16x16x128_f8f6f4 v[74:77], v[2:9], v[192:199], v[74:77], v189, v190 op_sel_hi:[0,0,0]
	v_mfma_scale_f32_16x16x128_f8f6f4 v[66:69], v[10:17], v[200:207], v[66:69], v189, v190 op_sel_hi:[0,0,0]
	v_mfma_scale_f32_16x16x128_f8f6f4 v[58:61], v[2:9], v[200:207], v[58:61], v189, v190 op_sel_hi:[0,0,0]
	v_mfma_scale_f32_16x16x128_f8f6f4 v[50:53], v[10:17], v[208:215], v[50:53], v189, v190 op_sel_hi:[0,0,0]
	v_mfma_scale_f32_16x16x128_f8f6f4 v[42:45], v[2:9], v[208:215], v[42:45], v189, v190 op_sel_hi:[0,0,0]
	v_mfma_scale_f32_16x16x128_f8f6f4 v[38:41], v[10:17], v[220:227], v[38:41], v189, v190 op_sel_hi:[0,0,0]
	v_mfma_scale_f32_16x16x128_f8f6f4 v[34:37], v[2:9], v[220:227], v[34:37], v189, v190 op_sel_hi:[0,0,0]
	s_setprio 1
	s_barrier
	s_add_i32 s80, 0, 0x18000
	s_add_i32 s81, 0, 0x1c000
	v_add_u32_e32 v14, s80, v184
	v_add_u32_e32 v30, s81, v184
	ds_read_b128 v[2:5], v14
	ds_read_b128 v[6:9], v14 offset:1024
	ds_read_b128 v[10:13], v14 offset:2048
	ds_read_b128 v[14:17], v14 offset:3072
	ds_read_b128 v[18:21], v30
	ds_read_b128 v[22:25], v30 offset:1024
	ds_read_b128 v[26:29], v30 offset:2048
	ds_read_b128 v[30:33], v30 offset:3072
	s_add_u32 s58, s58, 0xb0000
	s_addc_u32 s59, s59, 0
	s_mov_b32 m0, s63
	v_lshl_add_u64 v[216:217], s[58:59], 0, v[166:167]
	ds_read_b128 v[192:195], v188 offset:32768
	ds_read_b128 v[196:199], v188 offset:33792
	ds_read_b128 v[200:203], v188 offset:34816
	ds_read_b128 v[204:207], v188 offset:35840
	ds_read_b128 v[208:211], v188 offset:36864
	ds_read_b128 v[212:215], v188 offset:37888
	ds_read_b128 v[220:223], v188 offset:38912
	ds_read_b128 v[224:227], v188 offset:39936
	global_load_lds_dwordx4 v[216:217], off
	v_lshl_add_u64 v[216:217], s[58:59], 0, v[168:169]
	s_mov_b32 m0, s64
	s_nop 0
	global_load_lds_dwordx4 v[216:217], off
	s_waitcnt vmcnt(8)
	s_waitcnt lgkmcnt(0)
	s_barrier
	s_setprio 0
	s_waitcnt lgkmcnt(0)
	v_mfma_scale_f32_16x16x128_f8f6f4 v[158:161], v[2:9], v[192:199], v[158:161], v189, v190 op_sel_hi:[0,0,0]
	v_mfma_scale_f32_16x16x128_f8f6f4 v[154:157], v[10:17], v[192:199], v[154:157], v189, v190 op_sel_hi:[0,0,0]
	v_mfma_scale_f32_16x16x128_f8f6f4 v[150:153], v[2:9], v[200:207], v[150:153], v189, v190 op_sel_hi:[0,0,0]
	v_mfma_scale_f32_16x16x128_f8f6f4 v[142:145], v[10:17], v[200:207], v[142:145], v189, v190 op_sel_hi:[0,0,0]
	v_mfma_scale_f32_16x16x128_f8f6f4 v[134:137], v[2:9], v[208:215], v[134:137], v189, v190 op_sel_hi:[0,0,0]
	v_mfma_scale_f32_16x16x128_f8f6f4 v[126:129], v[10:17], v[208:215], v[126:129], v189, v190 op_sel_hi:[0,0,0]
	v_mfma_scale_f32_16x16x128_f8f6f4 v[118:121], v[2:9], v[220:227], v[118:121], v189, v190 op_sel_hi:[0,0,0]
	v_mfma_scale_f32_16x16x128_f8f6f4 v[110:113], v[10:17], v[220:227], v[110:113], v189, v190 op_sel_hi:[0,0,0]
	v_mfma_scale_f32_16x16x128_f8f6f4 v[146:149], v[18:25], v[192:199], v[146:149], v189, v190 op_sel_hi:[0,0,0]
	v_mfma_scale_f32_16x16x128_f8f6f4 v[138:141], v[26:33], v[192:199], v[138:141], v189, v190 op_sel_hi:[0,0,0]
	v_mfma_scale_f32_16x16x128_f8f6f4 v[130:133], v[18:25], v[200:207], v[130:133], v189, v190 op_sel_hi:[0,0,0]
	v_mfma_scale_f32_16x16x128_f8f6f4 v[122:125], v[26:33], v[200:207], v[122:125], v189, v190 op_sel_hi:[0,0,0]
	v_mfma_scale_f32_16x16x128_f8f6f4 v[114:117], v[18:25], v[208:215], v[114:117], v189, v190 op_sel_hi:[0,0,0]
	v_mfma_scale_f32_16x16x128_f8f6f4 v[106:109], v[26:33], v[208:215], v[106:109], v189, v190 op_sel_hi:[0,0,0]
	v_mfma_scale_f32_16x16x128_f8f6f4 v[102:105], v[18:25], v[220:227], v[102:105], v189, v190 op_sel_hi:[0,0,0]
	v_mfma_scale_f32_16x16x128_f8f6f4 v[98:101], v[26:33], v[220:227], v[98:101], v189, v190 op_sel_hi:[0,0,0]
	s_setprio 1
	s_barrier
	s_add_i32 s58, s80, s33
	v_lshl_add_u64 v[216:217], v[178:179], 0, s[24:25]
	s_mov_b32 m0, s58
	ds_read_b128 v[192:195], v188 offset:49152
	ds_read_b128 v[196:199], v188 offset:50176
	ds_read_b128 v[200:203], v188 offset:51200
	ds_read_b128 v[204:207], v188 offset:52224
	ds_read_b128 v[208:211], v188 offset:53248
	ds_read_b128 v[212:215], v188 offset:54272
	ds_read_b128 v[220:223], v188 offset:55296
	ds_read_b128 v[224:227], v188 offset:56320
	global_load_lds_dwordx4 v[216:217], off
	v_lshl_add_u64 v[216:217], v[178:179], 0, s[26:27]
	s_add_i32 m0, s58, 0x2000
	s_add_i32 s58, s81, s33
	global_load_lds_dwordx4 v[216:217], off
	v_lshl_add_u64 v[216:217], v[178:179], 0, s[38:39]
	s_mov_b32 m0, s58
	v_lshl_add_u64 v[178:179], v[178:179], 0, s[40:41]
	global_load_lds_dwordx4 v[216:217], off
	s_add_i32 m0, s58, 0x2000
	s_nop 0
	global_load_lds_dwordx4 v[178:179], off
	v_lshl_add_u64 v[178:179], v[180:181], 0, s[36:37]
	s_mov_b32 m0, s66
	s_nop 0
	global_load_lds_dwordx4 v[178:179], off
	v_lshl_add_u64 v[178:179], v[182:183], 0, s[36:37]
	s_mov_b32 m0, s67
	s_nop 0
	global_load_lds_dwordx4 v[178:179], off
	s_waitcnt vmcnt(8)
	s_waitcnt lgkmcnt(0)
	s_barrier
	s_setprio 0
	s_waitcnt lgkmcnt(0)
	v_mfma_scale_f32_16x16x128_f8f6f4 v[94:97], v[2:9], v[192:199], v[94:97], v189, v190 op_sel_hi:[0,0,0]
	v_mfma_scale_f32_16x16x128_f8f6f4 v[90:93], v[10:17], v[192:199], v[90:93], v189, v190 op_sel_hi:[0,0,0]
	v_mfma_scale_f32_16x16x128_f8f6f4 v[86:89], v[2:9], v[200:207], v[86:89], v189, v190 op_sel_hi:[0,0,0]
	v_mfma_scale_f32_16x16x128_f8f6f4 v[78:81], v[10:17], v[200:207], v[78:81], v189, v190 op_sel_hi:[0,0,0]
	v_mfma_scale_f32_16x16x128_f8f6f4 v[70:73], v[2:9], v[208:215], v[70:73], v189, v190 op_sel_hi:[0,0,0]
	v_mfma_scale_f32_16x16x128_f8f6f4 v[62:65], v[10:17], v[208:215], v[62:65], v189, v190 op_sel_hi:[0,0,0]
	v_mfma_scale_f32_16x16x128_f8f6f4 v[54:57], v[2:9], v[220:227], v[54:57], v189, v190 op_sel_hi:[0,0,0]
	v_mfma_scale_f32_16x16x128_f8f6f4 v[46:49], v[10:17], v[220:227], v[46:49], v189, v190 op_sel_hi:[0,0,0]
	v_mfma_scale_f32_16x16x128_f8f6f4 v[82:85], v[18:25], v[192:199], v[82:85], v189, v190 op_sel_hi:[0,0,0]
	v_mfma_scale_f32_16x16x128_f8f6f4 v[74:77], v[26:33], v[192:199], v[74:77], v189, v190 op_sel_hi:[0,0,0]
	v_mfma_scale_f32_16x16x128_f8f6f4 v[66:69], v[18:25], v[200:207], v[66:69], v189, v190 op_sel_hi:[0,0,0]
	v_mfma_scale_f32_16x16x128_f8f6f4 v[58:61], v[26:33], v[200:207], v[58:61], v189, v190 op_sel_hi:[0,0,0]
	v_mfma_scale_f32_16x16x128_f8f6f4 v[50:53], v[18:25], v[208:215], v[50:53], v189, v190 op_sel_hi:[0,0,0]
	v_mfma_scale_f32_16x16x128_f8f6f4 v[42:45], v[26:33], v[208:215], v[42:45], v189, v190 op_sel_hi:[0,0,0]
	v_mfma_scale_f32_16x16x128_f8f6f4 v[38:41], v[18:25], v[220:227], v[38:41], v189, v190 op_sel_hi:[0,0,0]
	v_mfma_scale_f32_16x16x128_f8f6f4 v[34:37], v[26:33], v[220:227], v[34:37], v189, v190 op_sel_hi:[0,0,0]
	s_setprio 1
	s_barrier
	s_add_i32 s53, s53, 2
	s_add_u32 s56, s56, 0x100
	s_addc_u32 s57, s57, 0
	s_cmp_gt_u32 s53, 41
	v_lshl_add_u64 v[176:177], v[176:177], 0, s[44:45]
	s_cbranch_scc0 .LBB0_1568
	s_and_b64 vcc, exec, s[42:43]
	s_cbranch_vccz .LBB0_1571
	s_barrier
